# speedup vs baseline: 1.0035x; 1.0035x over previous
.Lscan_enter_b_st:
	ds_read_b128 v[122:125], v192 offset:0
	ds_read_b64 v[126:127], v192 offset:16
	ds_read_b128 v[128:131], v192 offset:128
	ds_read_b64 v[132:133], v192 offset:144
	s_waitcnt vmcnt(8)
	global_load_dwordx4 v[146:149], v[196:197], off
	global_load_dwordx4 v[150:153], v[196:197], off offset:512
	global_load_dwordx4 v[154:157], v[196:197], off offset:1024
	v_lshl_add_u64 v[196:197], v[196:197], 0, s[42:43]
	s_nop 7
	s_waitcnt lgkmcnt(2)
	v_mfma_f32_16x16x128_f8f6f4 v[134:137], v[122:127], v[2:7], 0 cbsz:2 blgp:2
	v_mfma_f32_16x16x128_f8f6f4 v[138:141], v[122:127], v[14:19], 0 cbsz:2 blgp:2
	v_mfma_f32_16x16x128_f8f6f4 v[142:145], v[122:127], v[26:31], v[188:191] cbsz:2 blgp:2
	v_mfma_f32_16x16x128_f8f6f4 v[204:207], v[122:127], v[38:43], 0 cbsz:2 blgp:2
	v_mfma_f32_16x16x128_f8f6f4 v[208:211], v[122:127], v[50:55], 0 cbsz:2 blgp:2
	v_mfma_f32_16x16x128_f8f6f4 v[212:215], v[122:127], v[62:67], v[188:191] cbsz:2 blgp:2
	s_waitcnt lgkmcnt(0)
	v_mfma_f32_16x16x128_f8f6f4 v[134:137], v[128:133], v[8:13], v[134:137] cbsz:2 blgp:2
	v_mfma_f32_16x16x128_f8f6f4 v[204:207], v[128:133], v[44:49], v[204:207] cbsz:2 blgp:2
	v_mfma_f32_16x16x128_f8f6f4 v[138:141], v[128:133], v[20:25], v[138:141] cbsz:2 blgp:2
	v_mfma_f32_16x16x128_f8f6f4 v[208:211], v[128:133], v[56:61], v[208:211] cbsz:2 blgp:2
	v_mfma_f32_16x16x128_f8f6f4 v[142:145], v[128:133], v[32:37], v[142:145] cbsz:2 blgp:2
	v_mfma_f32_16x16x128_f8f6f4 v[212:215], v[128:133], v[68:73], v[212:215] cbsz:2 blgp:2
	v_cndmask_b32_e64 v158, v134, v204, s[4:5]
	v_cndmask_b32_e64 v159, v138, v208, s[4:5]
	v_fma_mix_f32 v158, v158, v1, v82 op_sel_hi:[0,0,1]
	v_fma_mix_f32 v159, v159, v99, v74 op_sel_hi:[0,0,1]
	v_exp_f32_e32 v158, v158
	v_exp_f32_e32 v159, v159
	v_fma_f32 v158, v158, v186, v186
	v_add_f32_e32 v159, 1.0, v159
	v_rcp_f32_e32 v158, v158
	v_rcp_f32_e32 v159, v159
	v_cndmask_b32_e64 v160, v142, v212, s[4:5]
	v_fma_mix_f32 v161, v158, v160, v78 op_sel_hi:[0,0,1]
	v_exp_f32_e32 v161, v161
	s_add_u32 s48, s48, s40
	v_add_f32_e32 v161, 1.0, v161
	v_rcp_f32_e32 v161, v161
	s_addc_u32 s49, s49, s41
	v_fma_f32 v162, v161, -2.0, 1.0
	v_sub_f32_e32 v163, v176, v162
	v_fma_f32 v176, v159, v163, v162
	v_fma_f32 v164, |v176|, s16, v117
	v_fma_f32 v165, |v176|, s17, v118
	v_fma_f32 v166, |v176|, s18, v119
	v_lshrrev_b32_e32 v167, 26, v176
	v_min3_u32 v164, v164, v165, v166
	v_bfi_b32 v168, 31, v164, v167
	s_nop 1
	v_mul_u32_u24_dpp v170, v168, v180 quad_perm:[1,2,3,3] row_mask:0xf bank_mask:0xf bound_ctrl:1
	v_mad_u32_u24 v171, v168, v181, v170
	ds_write_b8_d16_hi v184, v171 offset:544
	s_barrier
	global_store_short_d16_hi v185, v176, s[48:49]
	s_waitcnt lgkmcnt(0)
	s_barrier
	ds_read_b128 v[122:125], v192 offset:544
	ds_read_b64 v[126:127], v192 offset:560
	ds_read_b128 v[128:131], v192 offset:672
	ds_read_b64 v[132:133], v192 offset:688
	s_nop 7
	s_waitcnt lgkmcnt(2)
	v_mfma_f32_16x16x128_f8f6f4 v[134:137], v[122:127], v[2:7], 0 cbsz:2 blgp:2
	v_mfma_f32_16x16x128_f8f6f4 v[138:141], v[122:127], v[14:19], 0 cbsz:2 blgp:2
	v_mfma_f32_16x16x128_f8f6f4 v[142:145], v[122:127], v[26:31], v[188:191] cbsz:2 blgp:2
	v_mfma_f32_16x16x128_f8f6f4 v[204:207], v[122:127], v[38:43], 0 cbsz:2 blgp:2
	v_mfma_f32_16x16x128_f8f6f4 v[208:211], v[122:127], v[50:55], 0 cbsz:2 blgp:2
	v_mfma_f32_16x16x128_f8f6f4 v[212:215], v[122:127], v[62:67], v[188:191] cbsz:2 blgp:2
	s_waitcnt lgkmcnt(0)
	v_mfma_f32_16x16x128_f8f6f4 v[134:137], v[128:133], v[8:13], v[134:137] cbsz:2 blgp:2
	v_mfma_f32_16x16x128_f8f6f4 v[204:207], v[128:133], v[44:49], v[204:207] cbsz:2 blgp:2
	v_mfma_f32_16x16x128_f8f6f4 v[138:141], v[128:133], v[20:25], v[138:141] cbsz:2 blgp:2
	v_mfma_f32_16x16x128_f8f6f4 v[208:211], v[128:133], v[56:61], v[208:211] cbsz:2 blgp:2
	v_mfma_f32_16x16x128_f8f6f4 v[142:145], v[128:133], v[32:37], v[142:145] cbsz:2 blgp:2
	v_mfma_f32_16x16x128_f8f6f4 v[212:215], v[128:133], v[68:73], v[212:215] cbsz:2 blgp:2
	v_cndmask_b32_e64 v158, v134, v204, s[4:5]
	v_cndmask_b32_e64 v159, v138, v208, s[4:5]
	v_fma_mix_f32 v158, v158, v1, v82 op_sel:[0,0,1] op_sel_hi:[0,0,1]
	v_fma_mix_f32 v159, v159, v99, v74 op_sel:[0,0,1] op_sel_hi:[0,0,1]
	v_exp_f32_e32 v158, v158
	v_exp_f32_e32 v159, v159
	v_fma_f32 v158, v158, v186, v186
	v_add_f32_e32 v159, 1.0, v159
	v_rcp_f32_e32 v158, v158
	v_rcp_f32_e32 v159, v159
	v_cndmask_b32_e64 v160, v142, v212, s[4:5]
	v_fma_mix_f32 v161, v158, v160, v78 op_sel:[0,0,1] op_sel_hi:[0,0,1]
	v_exp_f32_e32 v161, v161
	s_add_u32 s48, s48, s40
	v_add_f32_e32 v161, 1.0, v161
	v_rcp_f32_e32 v161, v161
	s_addc_u32 s49, s49, s41
	v_fma_f32 v162, v161, -2.0, 1.0
	v_sub_f32_e32 v163, v176, v162
	v_fma_f32 v176, v159, v163, v162
	v_fma_f32 v164, |v176|, s16, v117
	v_fma_f32 v165, |v176|, s17, v118
	v_fma_f32 v166, |v176|, s18, v119
	v_lshrrev_b32_e32 v167, 26, v176
	v_min3_u32 v164, v164, v165, v166
	v_bfi_b32 v168, 31, v164, v167
	s_nop 1
	v_mul_u32_u24_dpp v170, v168, v180 quad_perm:[1,2,3,3] row_mask:0xf bank_mask:0xf bound_ctrl:1
	v_mad_u32_u24 v171, v168, v181, v170
	ds_write_b8_d16_hi v184, v171
	s_barrier
	global_store_short_d16_hi v185, v176, s[48:49]
	s_waitcnt lgkmcnt(0)
	s_barrier
	ds_read_b128 v[122:125], v192 offset:0
	ds_read_b64 v[126:127], v192 offset:16
	ds_read_b128 v[128:131], v192 offset:128
	ds_read_b64 v[132:133], v192 offset:144
	s_nop 7
	s_waitcnt lgkmcnt(2)
	v_mfma_f32_16x16x128_f8f6f4 v[134:137], v[122:127], v[2:7], 0 cbsz:2 blgp:2
	v_mfma_f32_16x16x128_f8f6f4 v[138:141], v[122:127], v[14:19], 0 cbsz:2 blgp:2
	v_mfma_f32_16x16x128_f8f6f4 v[142:145], v[122:127], v[26:31], v[188:191] cbsz:2 blgp:2
	v_mfma_f32_16x16x128_f8f6f4 v[204:207], v[122:127], v[38:43], 0 cbsz:2 blgp:2
	v_mfma_f32_16x16x128_f8f6f4 v[208:211], v[122:127], v[50:55], 0 cbsz:2 blgp:2
	v_mfma_f32_16x16x128_f8f6f4 v[212:215], v[122:127], v[62:67], v[188:191] cbsz:2 blgp:2
	s_waitcnt lgkmcnt(0)
	v_mfma_f32_16x16x128_f8f6f4 v[134:137], v[128:133], v[8:13], v[134:137] cbsz:2 blgp:2
	v_mfma_f32_16x16x128_f8f6f4 v[204:207], v[128:133], v[44:49], v[204:207] cbsz:2 blgp:2
	v_mfma_f32_16x16x128_f8f6f4 v[138:141], v[128:133], v[20:25], v[138:141] cbsz:2 blgp:2
	v_mfma_f32_16x16x128_f8f6f4 v[208:211], v[128:133], v[56:61], v[208:211] cbsz:2 blgp:2
	v_mfma_f32_16x16x128_f8f6f4 v[142:145], v[128:133], v[32:37], v[142:145] cbsz:2 blgp:2
	v_mfma_f32_16x16x128_f8f6f4 v[212:215], v[128:133], v[68:73], v[212:215] cbsz:2 blgp:2
	v_cndmask_b32_e64 v158, v134, v204, s[4:5]
	v_cndmask_b32_e64 v159, v138, v208, s[4:5]
	v_fma_mix_f32 v158, v158, v1, v83 op_sel_hi:[0,0,1]
	v_fma_mix_f32 v159, v159, v99, v75 op_sel_hi:[0,0,1]
	v_exp_f32_e32 v158, v158
	v_exp_f32_e32 v159, v159
	v_fma_f32 v158, v158, v186, v186
	v_add_f32_e32 v159, 1.0, v159
	v_rcp_f32_e32 v158, v158
	v_rcp_f32_e32 v159, v159
	v_cndmask_b32_e64 v160, v142, v212, s[4:5]
	v_fma_mix_f32 v161, v158, v160, v79 op_sel_hi:[0,0,1]
	v_exp_f32_e32 v161, v161
	s_add_u32 s48, s48, s40
	v_add_f32_e32 v161, 1.0, v161
	v_rcp_f32_e32 v161, v161
	s_addc_u32 s49, s49, s41
	v_fma_f32 v162, v161, -2.0, 1.0
	v_sub_f32_e32 v163, v176, v162
	v_fma_f32 v176, v159, v163, v162
	v_fma_f32 v164, |v176|, s16, v117
	v_fma_f32 v165, |v176|, s17, v118
	v_fma_f32 v166, |v176|, s18, v119
	v_lshrrev_b32_e32 v167, 26, v176
	v_min3_u32 v164, v164, v165, v166
	v_bfi_b32 v168, 31, v164, v167
	s_nop 1
	v_mul_u32_u24_dpp v170, v168, v180 quad_perm:[1,2,3,3] row_mask:0xf bank_mask:0xf bound_ctrl:1
	v_mad_u32_u24 v171, v168, v181, v170
	ds_write_b8_d16_hi v184, v171 offset:544
	s_barrier
	global_store_short_d16_hi v185, v176, s[48:49]
	s_waitcnt lgkmcnt(0)
	s_barrier
	ds_read_b128 v[122:125], v192 offset:544
	ds_read_b64 v[126:127], v192 offset:560
	ds_read_b128 v[128:131], v192 offset:672
	ds_read_b64 v[132:133], v192 offset:688
	s_nop 7
	s_waitcnt lgkmcnt(2)
	v_mfma_f32_16x16x128_f8f6f4 v[134:137], v[122:127], v[2:7], 0 cbsz:2 blgp:2
	v_mfma_f32_16x16x128_f8f6f4 v[138:141], v[122:127], v[14:19], 0 cbsz:2 blgp:2
	v_mfma_f32_16x16x128_f8f6f4 v[142:145], v[122:127], v[26:31], v[188:191] cbsz:2 blgp:2
	v_mfma_f32_16x16x128_f8f6f4 v[204:207], v[122:127], v[38:43], 0 cbsz:2 blgp:2
	v_mfma_f32_16x16x128_f8f6f4 v[208:211], v[122:127], v[50:55], 0 cbsz:2 blgp:2
	v_mfma_f32_16x16x128_f8f6f4 v[212:215], v[122:127], v[62:67], v[188:191] cbsz:2 blgp:2
	s_waitcnt lgkmcnt(0)
	v_mfma_f32_16x16x128_f8f6f4 v[134:137], v[128:133], v[8:13], v[134:137] cbsz:2 blgp:2
	v_mfma_f32_16x16x128_f8f6f4 v[204:207], v[128:133], v[44:49], v[204:207] cbsz:2 blgp:2
	v_mfma_f32_16x16x128_f8f6f4 v[138:141], v[128:133], v[20:25], v[138:141] cbsz:2 blgp:2
	v_mfma_f32_16x16x128_f8f6f4 v[208:211], v[128:133], v[56:61], v[208:211] cbsz:2 blgp:2
	v_mfma_f32_16x16x128_f8f6f4 v[142:145], v[128:133], v[32:37], v[142:145] cbsz:2 blgp:2
	v_mfma_f32_16x16x128_f8f6f4 v[212:215], v[128:133], v[68:73], v[212:215] cbsz:2 blgp:2
	v_cndmask_b32_e64 v158, v134, v204, s[4:5]
	v_cndmask_b32_e64 v159, v138, v208, s[4:5]
	v_fma_mix_f32 v158, v158, v1, v83 op_sel:[0,0,1] op_sel_hi:[0,0,1]
	v_fma_mix_f32 v159, v159, v99, v75 op_sel:[0,0,1] op_sel_hi:[0,0,1]
	v_exp_f32_e32 v158, v158
	v_exp_f32_e32 v159, v159
	v_fma_f32 v158, v158, v186, v186
	v_add_f32_e32 v159, 1.0, v159
	v_rcp_f32_e32 v158, v158
	v_rcp_f32_e32 v159, v159
	v_cndmask_b32_e64 v160, v142, v212, s[4:5]
	v_fma_mix_f32 v161, v158, v160, v79 op_sel:[0,0,1] op_sel_hi:[0,0,1]
	v_exp_f32_e32 v161, v161
	s_add_u32 s48, s48, s40
	v_add_f32_e32 v161, 1.0, v161
	v_rcp_f32_e32 v161, v161
	s_addc_u32 s49, s49, s41
	v_fma_f32 v162, v161, -2.0, 1.0
	v_sub_f32_e32 v163, v176, v162
	v_fma_f32 v176, v159, v163, v162
	v_fma_f32 v164, |v176|, s16, v117
	v_fma_f32 v165, |v176|, s17, v118
	v_fma_f32 v166, |v176|, s18, v119
	v_lshrrev_b32_e32 v167, 26, v176
	v_min3_u32 v164, v164, v165, v166
	v_bfi_b32 v168, 31, v164, v167
	s_nop 1
	v_mul_u32_u24_dpp v170, v168, v180 quad_perm:[1,2,3,3] row_mask:0xf bank_mask:0xf bound_ctrl:1
	v_mad_u32_u24 v171, v168, v181, v170
	ds_write_b8_d16_hi v184, v171
	s_barrier
	global_store_short_d16_hi v185, v176, s[48:49]
	s_waitcnt lgkmcnt(0)
	s_barrier
	ds_read_b128 v[122:125], v192 offset:0
	ds_read_b64 v[126:127], v192 offset:16
	ds_read_b128 v[128:131], v192 offset:128
	ds_read_b64 v[132:133], v192 offset:144
	s_nop 7
	s_waitcnt lgkmcnt(2)
	v_mfma_f32_16x16x128_f8f6f4 v[134:137], v[122:127], v[2:7], 0 cbsz:2 blgp:2
	v_mfma_f32_16x16x128_f8f6f4 v[138:141], v[122:127], v[14:19], 0 cbsz:2 blgp:2
	v_mfma_f32_16x16x128_f8f6f4 v[142:145], v[122:127], v[26:31], v[188:191] cbsz:2 blgp:2
	v_mfma_f32_16x16x128_f8f6f4 v[204:207], v[122:127], v[38:43], 0 cbsz:2 blgp:2
	v_mfma_f32_16x16x128_f8f6f4 v[208:211], v[122:127], v[50:55], 0 cbsz:2 blgp:2
	v_mfma_f32_16x16x128_f8f6f4 v[212:215], v[122:127], v[62:67], v[188:191] cbsz:2 blgp:2
	s_waitcnt lgkmcnt(0)
	v_mfma_f32_16x16x128_f8f6f4 v[134:137], v[128:133], v[8:13], v[134:137] cbsz:2 blgp:2
	v_mfma_f32_16x16x128_f8f6f4 v[204:207], v[128:133], v[44:49], v[204:207] cbsz:2 blgp:2
	v_mfma_f32_16x16x128_f8f6f4 v[138:141], v[128:133], v[20:25], v[138:141] cbsz:2 blgp:2
	v_mfma_f32_16x16x128_f8f6f4 v[208:211], v[128:133], v[56:61], v[208:211] cbsz:2 blgp:2
	v_mfma_f32_16x16x128_f8f6f4 v[142:145], v[128:133], v[32:37], v[142:145] cbsz:2 blgp:2
	v_mfma_f32_16x16x128_f8f6f4 v[212:215], v[128:133], v[68:73], v[212:215] cbsz:2 blgp:2
	v_cndmask_b32_e64 v158, v134, v204, s[4:5]
	v_cndmask_b32_e64 v159, v138, v208, s[4:5]
	v_fma_mix_f32 v158, v158, v1, v84 op_sel_hi:[0,0,1]
	v_fma_mix_f32 v159, v159, v99, v76 op_sel_hi:[0,0,1]
	v_exp_f32_e32 v158, v158
	v_exp_f32_e32 v159, v159
	v_fma_f32 v158, v158, v186, v186
	v_add_f32_e32 v159, 1.0, v159
	v_rcp_f32_e32 v158, v158
	v_rcp_f32_e32 v159, v159
	v_cndmask_b32_e64 v160, v142, v212, s[4:5]
	v_fma_mix_f32 v161, v158, v160, v80 op_sel_hi:[0,0,1]
	v_exp_f32_e32 v161, v161
	s_add_u32 s48, s48, s40
	v_add_f32_e32 v161, 1.0, v161
	v_rcp_f32_e32 v161, v161
	s_addc_u32 s49, s49, s41
	v_fma_f32 v162, v161, -2.0, 1.0
	v_sub_f32_e32 v163, v176, v162
	v_fma_f32 v176, v159, v163, v162
	v_fma_f32 v164, |v176|, s16, v117
	v_fma_f32 v165, |v176|, s17, v118
	v_fma_f32 v166, |v176|, s18, v119
	v_lshrrev_b32_e32 v167, 26, v176
	v_min3_u32 v164, v164, v165, v166
	v_bfi_b32 v168, 31, v164, v167
	s_nop 1
	v_mul_u32_u24_dpp v170, v168, v180 quad_perm:[1,2,3,3] row_mask:0xf bank_mask:0xf bound_ctrl:1
	v_mad_u32_u24 v171, v168, v181, v170
	ds_write_b8_d16_hi v184, v171 offset:544
	s_barrier
	global_store_short_d16_hi v185, v176, s[48:49]
	s_waitcnt lgkmcnt(0)
	s_barrier
	ds_read_b128 v[122:125], v192 offset:544
	ds_read_b64 v[126:127], v192 offset:560
	ds_read_b128 v[128:131], v192 offset:672
	ds_read_b64 v[132:133], v192 offset:688
	s_nop 7
	s_waitcnt lgkmcnt(2)
	v_mfma_f32_16x16x128_f8f6f4 v[134:137], v[122:127], v[2:7], 0 cbsz:2 blgp:2
	v_mfma_f32_16x16x128_f8f6f4 v[138:141], v[122:127], v[14:19], 0 cbsz:2 blgp:2
	v_mfma_f32_16x16x128_f8f6f4 v[142:145], v[122:127], v[26:31], v[188:191] cbsz:2 blgp:2
	v_mfma_f32_16x16x128_f8f6f4 v[204:207], v[122:127], v[38:43], 0 cbsz:2 blgp:2
	v_mfma_f32_16x16x128_f8f6f4 v[208:211], v[122:127], v[50:55], 0 cbsz:2 blgp:2
	v_mfma_f32_16x16x128_f8f6f4 v[212:215], v[122:127], v[62:67], v[188:191] cbsz:2 blgp:2
	s_waitcnt lgkmcnt(0)
	v_mfma_f32_16x16x128_f8f6f4 v[134:137], v[128:133], v[8:13], v[134:137] cbsz:2 blgp:2
	v_mfma_f32_16x16x128_f8f6f4 v[204:207], v[128:133], v[44:49], v[204:207] cbsz:2 blgp:2
	v_mfma_f32_16x16x128_f8f6f4 v[138:141], v[128:133], v[20:25], v[138:141] cbsz:2 blgp:2
	v_mfma_f32_16x16x128_f8f6f4 v[208:211], v[128:133], v[56:61], v[208:211] cbsz:2 blgp:2
	v_mfma_f32_16x16x128_f8f6f4 v[142:145], v[128:133], v[32:37], v[142:145] cbsz:2 blgp:2
	v_mfma_f32_16x16x128_f8f6f4 v[212:215], v[128:133], v[68:73], v[212:215] cbsz:2 blgp:2
	v_cndmask_b32_e64 v158, v134, v204, s[4:5]
	v_cndmask_b32_e64 v159, v138, v208, s[4:5]
	v_fma_mix_f32 v158, v158, v1, v84 op_sel:[0,0,1] op_sel_hi:[0,0,1]
	v_fma_mix_f32 v159, v159, v99, v76 op_sel:[0,0,1] op_sel_hi:[0,0,1]
	v_exp_f32_e32 v158, v158
	v_exp_f32_e32 v159, v159
	v_fma_f32 v158, v158, v186, v186
	v_add_f32_e32 v159, 1.0, v159
	v_rcp_f32_e32 v158, v158
	v_rcp_f32_e32 v159, v159
	v_cndmask_b32_e64 v160, v142, v212, s[4:5]
	v_fma_mix_f32 v161, v158, v160, v80 op_sel:[0,0,1] op_sel_hi:[0,0,1]
	v_exp_f32_e32 v161, v161
	s_add_u32 s48, s48, s40
	v_add_f32_e32 v161, 1.0, v161
	v_rcp_f32_e32 v161, v161
	s_addc_u32 s49, s49, s41
	v_fma_f32 v162, v161, -2.0, 1.0
	v_sub_f32_e32 v163, v176, v162
	v_fma_f32 v176, v159, v163, v162
	v_fma_f32 v164, |v176|, s16, v117
	v_fma_f32 v165, |v176|, s17, v118
	v_fma_f32 v166, |v176|, s18, v119
	v_lshrrev_b32_e32 v167, 26, v176
	v_min3_u32 v164, v164, v165, v166
	v_bfi_b32 v168, 31, v164, v167
	s_nop 1
	v_mul_u32_u24_dpp v170, v168, v180 quad_perm:[1,2,3,3] row_mask:0xf bank_mask:0xf bound_ctrl:1
	v_mad_u32_u24 v171, v168, v181, v170
	ds_write_b8_d16_hi v184, v171
	s_barrier
	global_store_short_d16_hi v185, v176, s[48:49]
	s_waitcnt lgkmcnt(0)
	s_barrier
	ds_read_b128 v[122:125], v192 offset:0
	ds_read_b64 v[126:127], v192 offset:16
	ds_read_b128 v[128:131], v192 offset:128
	ds_read_b64 v[132:133], v192 offset:144
	s_nop 7
	s_waitcnt lgkmcnt(2)
	v_mfma_f32_16x16x128_f8f6f4 v[134:137], v[122:127], v[2:7], 0 cbsz:2 blgp:2
	v_mfma_f32_16x16x128_f8f6f4 v[138:141], v[122:127], v[14:19], 0 cbsz:2 blgp:2
	v_mfma_f32_16x16x128_f8f6f4 v[142:145], v[122:127], v[26:31], v[188:191] cbsz:2 blgp:2
	v_mfma_f32_16x16x128_f8f6f4 v[204:207], v[122:127], v[38:43], 0 cbsz:2 blgp:2
	v_mfma_f32_16x16x128_f8f6f4 v[208:211], v[122:127], v[50:55], 0 cbsz:2 blgp:2
	v_mfma_f32_16x16x128_f8f6f4 v[212:215], v[122:127], v[62:67], v[188:191] cbsz:2 blgp:2
	s_waitcnt lgkmcnt(0)
	v_mfma_f32_16x16x128_f8f6f4 v[134:137], v[128:133], v[8:13], v[134:137] cbsz:2 blgp:2
	v_mfma_f32_16x16x128_f8f6f4 v[204:207], v[128:133], v[44:49], v[204:207] cbsz:2 blgp:2
	v_mfma_f32_16x16x128_f8f6f4 v[138:141], v[128:133], v[20:25], v[138:141] cbsz:2 blgp:2
	v_mfma_f32_16x16x128_f8f6f4 v[208:211], v[128:133], v[56:61], v[208:211] cbsz:2 blgp:2
	v_mfma_f32_16x16x128_f8f6f4 v[142:145], v[128:133], v[32:37], v[142:145] cbsz:2 blgp:2
	v_mfma_f32_16x16x128_f8f6f4 v[212:215], v[128:133], v[68:73], v[212:215] cbsz:2 blgp:2
	v_cndmask_b32_e64 v158, v134, v204, s[4:5]
	v_cndmask_b32_e64 v159, v138, v208, s[4:5]
	v_fma_mix_f32 v158, v158, v1, v85 op_sel_hi:[0,0,1]
	v_fma_mix_f32 v159, v159, v99, v77 op_sel_hi:[0,0,1]
	v_exp_f32_e32 v158, v158
	v_exp_f32_e32 v159, v159
	v_fma_f32 v158, v158, v186, v186
	v_add_f32_e32 v159, 1.0, v159
	v_rcp_f32_e32 v158, v158
	v_rcp_f32_e32 v159, v159
	v_cndmask_b32_e64 v160, v142, v212, s[4:5]
	v_fma_mix_f32 v161, v158, v160, v81 op_sel_hi:[0,0,1]
	v_exp_f32_e32 v161, v161
	s_add_u32 s48, s48, s40
	v_add_f32_e32 v161, 1.0, v161
	v_rcp_f32_e32 v161, v161
	s_addc_u32 s49, s49, s41
	v_fma_f32 v162, v161, -2.0, 1.0
	v_sub_f32_e32 v163, v176, v162
	v_fma_f32 v176, v159, v163, v162
	v_fma_f32 v164, |v176|, s16, v117
	v_fma_f32 v165, |v176|, s17, v118
	v_fma_f32 v166, |v176|, s18, v119
	v_lshrrev_b32_e32 v167, 26, v176
	v_min3_u32 v164, v164, v165, v166
	v_bfi_b32 v168, 31, v164, v167
	s_nop 1
	v_mul_u32_u24_dpp v170, v168, v180 quad_perm:[1,2,3,3] row_mask:0xf bank_mask:0xf bound_ctrl:1
	v_mad_u32_u24 v171, v168, v181, v170
	ds_write_b8_d16_hi v184, v171 offset:544
	s_barrier
	global_store_short_d16_hi v185, v176, s[48:49]
	s_waitcnt lgkmcnt(0)
	s_barrier
	ds_read_b128 v[122:125], v192 offset:544
	ds_read_b64 v[126:127], v192 offset:560
	ds_read_b128 v[128:131], v192 offset:672
	ds_read_b64 v[132:133], v192 offset:688
	s_nop 7
	s_waitcnt lgkmcnt(2)
	v_mfma_f32_16x16x128_f8f6f4 v[134:137], v[122:127], v[2:7], 0 cbsz:2 blgp:2
	v_mfma_f32_16x16x128_f8f6f4 v[138:141], v[122:127], v[14:19], 0 cbsz:2 blgp:2
	v_mfma_f32_16x16x128_f8f6f4 v[142:145], v[122:127], v[26:31], v[188:191] cbsz:2 blgp:2
	v_mfma_f32_16x16x128_f8f6f4 v[204:207], v[122:127], v[38:43], 0 cbsz:2 blgp:2
	v_mfma_f32_16x16x128_f8f6f4 v[208:211], v[122:127], v[50:55], 0 cbsz:2 blgp:2
	v_mfma_f32_16x16x128_f8f6f4 v[212:215], v[122:127], v[62:67], v[188:191] cbsz:2 blgp:2
	s_waitcnt lgkmcnt(0)
	v_mfma_f32_16x16x128_f8f6f4 v[134:137], v[128:133], v[8:13], v[134:137] cbsz:2 blgp:2
	v_mfma_f32_16x16x128_f8f6f4 v[204:207], v[128:133], v[44:49], v[204:207] cbsz:2 blgp:2
	v_mfma_f32_16x16x128_f8f6f4 v[138:141], v[128:133], v[20:25], v[138:141] cbsz:2 blgp:2
	v_mfma_f32_16x16x128_f8f6f4 v[208:211], v[128:133], v[56:61], v[208:211] cbsz:2 blgp:2
	v_mfma_f32_16x16x128_f8f6f4 v[142:145], v[128:133], v[32:37], v[142:145] cbsz:2 blgp:2
	v_mfma_f32_16x16x128_f8f6f4 v[212:215], v[128:133], v[68:73], v[212:215] cbsz:2 blgp:2
	v_cndmask_b32_e64 v158, v134, v204, s[4:5]
	v_cndmask_b32_e64 v159, v138, v208, s[4:5]
	v_fma_mix_f32 v158, v158, v1, v85 op_sel:[0,0,1] op_sel_hi:[0,0,1]
	v_fma_mix_f32 v159, v159, v99, v77 op_sel:[0,0,1] op_sel_hi:[0,0,1]
	v_exp_f32_e32 v158, v158
	v_exp_f32_e32 v159, v159
	v_fma_f32 v158, v158, v186, v186
	v_add_f32_e32 v159, 1.0, v159
	v_rcp_f32_e32 v158, v158
	v_rcp_f32_e32 v159, v159
	v_cndmask_b32_e64 v160, v142, v212, s[4:5]
	v_fma_mix_f32 v161, v158, v160, v81 op_sel:[0,0,1] op_sel_hi:[0,0,1]
	v_exp_f32_e32 v161, v161
	s_add_u32 s48, s48, s40
	v_add_f32_e32 v161, 1.0, v161
	v_rcp_f32_e32 v161, v161
	s_addc_u32 s49, s49, s41
	v_fma_f32 v162, v161, -2.0, 1.0
	v_sub_f32_e32 v163, v176, v162
	v_fma_f32 v176, v159, v163, v162
	v_fma_f32 v164, |v176|, s16, v117
	v_fma_f32 v165, |v176|, s17, v118
	v_fma_f32 v166, |v176|, s18, v119
	v_lshrrev_b32_e32 v167, 26, v176
	v_min3_u32 v164, v164, v165, v166
	v_bfi_b32 v168, 31, v164, v167
	s_nop 1
	v_mul_u32_u24_dpp v170, v168, v180 quad_perm:[1,2,3,3] row_mask:0xf bank_mask:0xf bound_ctrl:1
	v_mad_u32_u24 v171, v168, v181, v170
	ds_write_b8_d16_hi v184, v171
	s_barrier
	global_store_short_d16_hi v185, v176, s[48:49]
	s_waitcnt lgkmcnt(0)
	s_barrier
	ds_read_b128 v[122:125], v192 offset:0
	ds_read_b64 v[126:127], v192 offset:16
	ds_read_b128 v[128:131], v192 offset:128
	ds_read_b64 v[132:133], v192 offset:144
	s_waitcnt vmcnt(8)
	global_load_dwordx4 v[82:85], v[196:197], off
	global_load_dwordx4 v[74:77], v[196:197], off offset:512
	global_load_dwordx4 v[78:81], v[196:197], off offset:1024
	v_lshl_add_u64 v[196:197], v[196:197], 0, s[42:43]
	s_nop 7
	s_waitcnt lgkmcnt(2)
	v_mfma_f32_16x16x128_f8f6f4 v[134:137], v[122:127], v[2:7], 0 cbsz:2 blgp:2
	v_mfma_f32_16x16x128_f8f6f4 v[138:141], v[122:127], v[14:19], 0 cbsz:2 blgp:2
	v_mfma_f32_16x16x128_f8f6f4 v[142:145], v[122:127], v[26:31], v[188:191] cbsz:2 blgp:2
	v_mfma_f32_16x16x128_f8f6f4 v[204:207], v[122:127], v[38:43], 0 cbsz:2 blgp:2
	v_mfma_f32_16x16x128_f8f6f4 v[208:211], v[122:127], v[50:55], 0 cbsz:2 blgp:2
	v_mfma_f32_16x16x128_f8f6f4 v[212:215], v[122:127], v[62:67], v[188:191] cbsz:2 blgp:2
	s_waitcnt lgkmcnt(0)
	v_mfma_f32_16x16x128_f8f6f4 v[134:137], v[128:133], v[8:13], v[134:137] cbsz:2 blgp:2
	v_mfma_f32_16x16x128_f8f6f4 v[204:207], v[128:133], v[44:49], v[204:207] cbsz:2 blgp:2
	v_mfma_f32_16x16x128_f8f6f4 v[138:141], v[128:133], v[20:25], v[138:141] cbsz:2 blgp:2
	v_mfma_f32_16x16x128_f8f6f4 v[208:211], v[128:133], v[56:61], v[208:211] cbsz:2 blgp:2
	v_mfma_f32_16x16x128_f8f6f4 v[142:145], v[128:133], v[32:37], v[142:145] cbsz:2 blgp:2
	v_mfma_f32_16x16x128_f8f6f4 v[212:215], v[128:133], v[68:73], v[212:215] cbsz:2 blgp:2
	v_cndmask_b32_e64 v158, v134, v204, s[4:5]
	v_cndmask_b32_e64 v159, v138, v208, s[4:5]
	v_fma_mix_f32 v158, v158, v1, v146 op_sel_hi:[0,0,1]
	v_fma_mix_f32 v159, v159, v99, v150 op_sel_hi:[0,0,1]
	v_exp_f32_e32 v158, v158
	v_exp_f32_e32 v159, v159
	v_fma_f32 v158, v158, v186, v186
	v_add_f32_e32 v159, 1.0, v159
	v_rcp_f32_e32 v158, v158
	v_rcp_f32_e32 v159, v159
	v_cndmask_b32_e64 v160, v142, v212, s[4:5]
	v_fma_mix_f32 v161, v158, v160, v154 op_sel_hi:[0,0,1]
	v_exp_f32_e32 v161, v161
	s_add_u32 s48, s48, s40
	v_add_f32_e32 v161, 1.0, v161
	v_rcp_f32_e32 v161, v161
	s_addc_u32 s49, s49, s41
	v_fma_f32 v162, v161, -2.0, 1.0
	v_sub_f32_e32 v163, v176, v162
	v_fma_f32 v176, v159, v163, v162
	v_fma_f32 v164, |v176|, s16, v117
	v_fma_f32 v165, |v176|, s17, v118
	v_fma_f32 v166, |v176|, s18, v119
	v_lshrrev_b32_e32 v167, 26, v176
	v_min3_u32 v164, v164, v165, v166
	v_bfi_b32 v168, 31, v164, v167
	s_nop 1
	v_mul_u32_u24_dpp v170, v168, v180 quad_perm:[1,2,3,3] row_mask:0xf bank_mask:0xf bound_ctrl:1
	v_mad_u32_u24 v171, v168, v181, v170
	ds_write_b8_d16_hi v184, v171 offset:544
	s_barrier
	global_store_short_d16_hi v185, v176, s[48:49]
	s_waitcnt lgkmcnt(0)
	s_barrier
	ds_read_b128 v[122:125], v192 offset:544
	ds_read_b64 v[126:127], v192 offset:560
	ds_read_b128 v[128:131], v192 offset:672
	ds_read_b64 v[132:133], v192 offset:688
	s_nop 7
	s_waitcnt lgkmcnt(2)
	v_mfma_f32_16x16x128_f8f6f4 v[134:137], v[122:127], v[2:7], 0 cbsz:2 blgp:2
	v_mfma_f32_16x16x128_f8f6f4 v[138:141], v[122:127], v[14:19], 0 cbsz:2 blgp:2
	v_mfma_f32_16x16x128_f8f6f4 v[142:145], v[122:127], v[26:31], v[188:191] cbsz:2 blgp:2
	v_mfma_f32_16x16x128_f8f6f4 v[204:207], v[122:127], v[38:43], 0 cbsz:2 blgp:2
	v_mfma_f32_16x16x128_f8f6f4 v[208:211], v[122:127], v[50:55], 0 cbsz:2 blgp:2
	v_mfma_f32_16x16x128_f8f6f4 v[212:215], v[122:127], v[62:67], v[188:191] cbsz:2 blgp:2
	s_waitcnt lgkmcnt(0)
	v_mfma_f32_16x16x128_f8f6f4 v[134:137], v[128:133], v[8:13], v[134:137] cbsz:2 blgp:2
	v_mfma_f32_16x16x128_f8f6f4 v[204:207], v[128:133], v[44:49], v[204:207] cbsz:2 blgp:2
	v_mfma_f32_16x16x128_f8f6f4 v[138:141], v[128:133], v[20:25], v[138:141] cbsz:2 blgp:2
	v_mfma_f32_16x16x128_f8f6f4 v[208:211], v[128:133], v[56:61], v[208:211] cbsz:2 blgp:2
	v_mfma_f32_16x16x128_f8f6f4 v[142:145], v[128:133], v[32:37], v[142:145] cbsz:2 blgp:2
	v_mfma_f32_16x16x128_f8f6f4 v[212:215], v[128:133], v[68:73], v[212:215] cbsz:2 blgp:2
	v_cndmask_b32_e64 v158, v134, v204, s[4:5]
	v_cndmask_b32_e64 v159, v138, v208, s[4:5]
	v_fma_mix_f32 v158, v158, v1, v146 op_sel:[0,0,1] op_sel_hi:[0,0,1]
	v_fma_mix_f32 v159, v159, v99, v150 op_sel:[0,0,1] op_sel_hi:[0,0,1]
	v_exp_f32_e32 v158, v158
	v_exp_f32_e32 v159, v159
	v_fma_f32 v158, v158, v186, v186
	v_add_f32_e32 v159, 1.0, v159
	v_rcp_f32_e32 v158, v158
	v_rcp_f32_e32 v159, v159
	v_cndmask_b32_e64 v160, v142, v212, s[4:5]
	v_fma_mix_f32 v161, v158, v160, v154 op_sel:[0,0,1] op_sel_hi:[0,0,1]
	v_exp_f32_e32 v161, v161
	s_add_u32 s48, s48, s40
	v_add_f32_e32 v161, 1.0, v161
	v_rcp_f32_e32 v161, v161
	s_addc_u32 s49, s49, s41
	v_fma_f32 v162, v161, -2.0, 1.0
	v_sub_f32_e32 v163, v176, v162
	v_fma_f32 v176, v159, v163, v162
	v_fma_f32 v164, |v176|, s16, v117
	v_fma_f32 v165, |v176|, s17, v118
	v_fma_f32 v166, |v176|, s18, v119
	v_lshrrev_b32_e32 v167, 26, v176
	v_min3_u32 v164, v164, v165, v166
	v_bfi_b32 v168, 31, v164, v167
	s_nop 1
	v_mul_u32_u24_dpp v170, v168, v180 quad_perm:[1,2,3,3] row_mask:0xf bank_mask:0xf bound_ctrl:1
	v_mad_u32_u24 v171, v168, v181, v170
	ds_write_b8_d16_hi v184, v171
	s_barrier
	global_store_short_d16_hi v185, v176, s[48:49]
	s_waitcnt lgkmcnt(0)
	s_barrier
	ds_read_b128 v[122:125], v192 offset:0
	ds_read_b64 v[126:127], v192 offset:16
	ds_read_b128 v[128:131], v192 offset:128
	ds_read_b64 v[132:133], v192 offset:144
	s_nop 7
	s_waitcnt lgkmcnt(2)
	v_mfma_f32_16x16x128_f8f6f4 v[134:137], v[122:127], v[2:7], 0 cbsz:2 blgp:2
	v_mfma_f32_16x16x128_f8f6f4 v[138:141], v[122:127], v[14:19], 0 cbsz:2 blgp:2
	v_mfma_f32_16x16x128_f8f6f4 v[142:145], v[122:127], v[26:31], v[188:191] cbsz:2 blgp:2
	v_mfma_f32_16x16x128_f8f6f4 v[204:207], v[122:127], v[38:43], 0 cbsz:2 blgp:2
	v_mfma_f32_16x16x128_f8f6f4 v[208:211], v[122:127], v[50:55], 0 cbsz:2 blgp:2
	v_mfma_f32_16x16x128_f8f6f4 v[212:215], v[122:127], v[62:67], v[188:191] cbsz:2 blgp:2
	s_waitcnt lgkmcnt(0)
	v_mfma_f32_16x16x128_f8f6f4 v[134:137], v[128:133], v[8:13], v[134:137] cbsz:2 blgp:2
	v_mfma_f32_16x16x128_f8f6f4 v[204:207], v[128:133], v[44:49], v[204:207] cbsz:2 blgp:2
	v_mfma_f32_16x16x128_f8f6f4 v[138:141], v[128:133], v[20:25], v[138:141] cbsz:2 blgp:2
	v_mfma_f32_16x16x128_f8f6f4 v[208:211], v[128:133], v[56:61], v[208:211] cbsz:2 blgp:2
	v_mfma_f32_16x16x128_f8f6f4 v[142:145], v[128:133], v[32:37], v[142:145] cbsz:2 blgp:2
	v_mfma_f32_16x16x128_f8f6f4 v[212:215], v[128:133], v[68:73], v[212:215] cbsz:2 blgp:2
	v_cndmask_b32_e64 v158, v134, v204, s[4:5]
	v_cndmask_b32_e64 v159, v138, v208, s[4:5]
	v_fma_mix_f32 v158, v158, v1, v147 op_sel_hi:[0,0,1]
	v_fma_mix_f32 v159, v159, v99, v151 op_sel_hi:[0,0,1]
	v_exp_f32_e32 v158, v158
	v_exp_f32_e32 v159, v159
	v_fma_f32 v158, v158, v186, v186
	v_add_f32_e32 v159, 1.0, v159
	v_rcp_f32_e32 v158, v158
	v_rcp_f32_e32 v159, v159
	v_cndmask_b32_e64 v160, v142, v212, s[4:5]
	v_fma_mix_f32 v161, v158, v160, v155 op_sel_hi:[0,0,1]
	v_exp_f32_e32 v161, v161
	s_add_u32 s48, s48, s40
	v_add_f32_e32 v161, 1.0, v161
	v_rcp_f32_e32 v161, v161
	s_addc_u32 s49, s49, s41
	v_fma_f32 v162, v161, -2.0, 1.0
	v_sub_f32_e32 v163, v176, v162
	v_fma_f32 v176, v159, v163, v162
	v_fma_f32 v164, |v176|, s16, v117
	v_fma_f32 v165, |v176|, s17, v118
	v_fma_f32 v166, |v176|, s18, v119
	v_lshrrev_b32_e32 v167, 26, v176
	v_min3_u32 v164, v164, v165, v166
	v_bfi_b32 v168, 31, v164, v167
	s_nop 1
	v_mul_u32_u24_dpp v170, v168, v180 quad_perm:[1,2,3,3] row_mask:0xf bank_mask:0xf bound_ctrl:1
	v_mad_u32_u24 v171, v168, v181, v170
	ds_write_b8_d16_hi v184, v171 offset:544
	s_barrier
	global_store_short_d16_hi v185, v176, s[48:49]
	s_waitcnt lgkmcnt(0)
	s_barrier
	ds_read_b128 v[122:125], v192 offset:544
	ds_read_b64 v[126:127], v192 offset:560
	ds_read_b128 v[128:131], v192 offset:672
	ds_read_b64 v[132:133], v192 offset:688
	s_nop 7
	s_waitcnt lgkmcnt(2)
	v_mfma_f32_16x16x128_f8f6f4 v[134:137], v[122:127], v[2:7], 0 cbsz:2 blgp:2
	v_mfma_f32_16x16x128_f8f6f4 v[138:141], v[122:127], v[14:19], 0 cbsz:2 blgp:2
	v_mfma_f32_16x16x128_f8f6f4 v[142:145], v[122:127], v[26:31], v[188:191] cbsz:2 blgp:2
	v_mfma_f32_16x16x128_f8f6f4 v[204:207], v[122:127], v[38:43], 0 cbsz:2 blgp:2
	v_mfma_f32_16x16x128_f8f6f4 v[208:211], v[122:127], v[50:55], 0 cbsz:2 blgp:2
	v_mfma_f32_16x16x128_f8f6f4 v[212:215], v[122:127], v[62:67], v[188:191] cbsz:2 blgp:2
	s_waitcnt lgkmcnt(0)
	v_mfma_f32_16x16x128_f8f6f4 v[134:137], v[128:133], v[8:13], v[134:137] cbsz:2 blgp:2
	v_mfma_f32_16x16x128_f8f6f4 v[204:207], v[128:133], v[44:49], v[204:207] cbsz:2 blgp:2
	v_mfma_f32_16x16x128_f8f6f4 v[138:141], v[128:133], v[20:25], v[138:141] cbsz:2 blgp:2
	v_mfma_f32_16x16x128_f8f6f4 v[208:211], v[128:133], v[56:61], v[208:211] cbsz:2 blgp:2
	v_mfma_f32_16x16x128_f8f6f4 v[142:145], v[128:133], v[32:37], v[142:145] cbsz:2 blgp:2
	v_mfma_f32_16x16x128_f8f6f4 v[212:215], v[128:133], v[68:73], v[212:215] cbsz:2 blgp:2
	v_cndmask_b32_e64 v158, v134, v204, s[4:5]
	v_cndmask_b32_e64 v159, v138, v208, s[4:5]
	v_fma_mix_f32 v158, v158, v1, v147 op_sel:[0,0,1] op_sel_hi:[0,0,1]
	v_fma_mix_f32 v159, v159, v99, v151 op_sel:[0,0,1] op_sel_hi:[0,0,1]
	v_exp_f32_e32 v158, v158
	v_exp_f32_e32 v159, v159
	v_fma_f32 v158, v158, v186, v186
	v_add_f32_e32 v159, 1.0, v159
	v_rcp_f32_e32 v158, v158
	v_rcp_f32_e32 v159, v159
	v_cndmask_b32_e64 v160, v142, v212, s[4:5]
	v_fma_mix_f32 v161, v158, v160, v155 op_sel:[0,0,1] op_sel_hi:[0,0,1]
	v_exp_f32_e32 v161, v161
	s_add_u32 s48, s48, s40
	v_add_f32_e32 v161, 1.0, v161
	v_rcp_f32_e32 v161, v161
	s_addc_u32 s49, s49, s41
	v_fma_f32 v162, v161, -2.0, 1.0
	v_sub_f32_e32 v163, v176, v162
	v_fma_f32 v176, v159, v163, v162
	v_fma_f32 v164, |v176|, s16, v117
	v_fma_f32 v165, |v176|, s17, v118
	v_fma_f32 v166, |v176|, s18, v119
	v_lshrrev_b32_e32 v167, 26, v176
	v_min3_u32 v164, v164, v165, v166
	v_bfi_b32 v168, 31, v164, v167
	s_nop 1
	v_mul_u32_u24_dpp v170, v168, v180 quad_perm:[1,2,3,3] row_mask:0xf bank_mask:0xf bound_ctrl:1
	v_mad_u32_u24 v171, v168, v181, v170
	ds_write_b8_d16_hi v184, v171
	s_barrier
	global_store_short_d16_hi v185, v176, s[48:49]
	s_waitcnt lgkmcnt(0)
	s_barrier
	ds_read_b128 v[122:125], v192 offset:0
	ds_read_b64 v[126:127], v192 offset:16
	ds_read_b128 v[128:131], v192 offset:128
	ds_read_b64 v[132:133], v192 offset:144
	s_nop 7
	s_waitcnt lgkmcnt(2)
	v_mfma_f32_16x16x128_f8f6f4 v[134:137], v[122:127], v[2:7], 0 cbsz:2 blgp:2
	v_mfma_f32_16x16x128_f8f6f4 v[138:141], v[122:127], v[14:19], 0 cbsz:2 blgp:2
	v_mfma_f32_16x16x128_f8f6f4 v[142:145], v[122:127], v[26:31], v[188:191] cbsz:2 blgp:2
	v_mfma_f32_16x16x128_f8f6f4 v[204:207], v[122:127], v[38:43], 0 cbsz:2 blgp:2
	v_mfma_f32_16x16x128_f8f6f4 v[208:211], v[122:127], v[50:55], 0 cbsz:2 blgp:2
	v_mfma_f32_16x16x128_f8f6f4 v[212:215], v[122:127], v[62:67], v[188:191] cbsz:2 blgp:2
	s_waitcnt lgkmcnt(0)
	v_mfma_f32_16x16x128_f8f6f4 v[134:137], v[128:133], v[8:13], v[134:137] cbsz:2 blgp:2
	v_mfma_f32_16x16x128_f8f6f4 v[204:207], v[128:133], v[44:49], v[204:207] cbsz:2 blgp:2
	v_mfma_f32_16x16x128_f8f6f4 v[138:141], v[128:133], v[20:25], v[138:141] cbsz:2 blgp:2
	v_mfma_f32_16x16x128_f8f6f4 v[208:211], v[128:133], v[56:61], v[208:211] cbsz:2 blgp:2
	v_mfma_f32_16x16x128_f8f6f4 v[142:145], v[128:133], v[32:37], v[142:145] cbsz:2 blgp:2
	v_mfma_f32_16x16x128_f8f6f4 v[212:215], v[128:133], v[68:73], v[212:215] cbsz:2 blgp:2
	v_cndmask_b32_e64 v158, v134, v204, s[4:5]
	v_cndmask_b32_e64 v159, v138, v208, s[4:5]
	v_fma_mix_f32 v158, v158, v1, v148 op_sel_hi:[0,0,1]
	v_fma_mix_f32 v159, v159, v99, v152 op_sel_hi:[0,0,1]
	v_exp_f32_e32 v158, v158
	v_exp_f32_e32 v159, v159
	v_fma_f32 v158, v158, v186, v186
	v_add_f32_e32 v159, 1.0, v159
	v_rcp_f32_e32 v158, v158
	v_rcp_f32_e32 v159, v159
	v_cndmask_b32_e64 v160, v142, v212, s[4:5]
	v_fma_mix_f32 v161, v158, v160, v156 op_sel_hi:[0,0,1]
	v_exp_f32_e32 v161, v161
	s_add_u32 s48, s48, s40
	v_add_f32_e32 v161, 1.0, v161
	v_rcp_f32_e32 v161, v161
	s_addc_u32 s49, s49, s41
	v_fma_f32 v162, v161, -2.0, 1.0
	v_sub_f32_e32 v163, v176, v162
	v_fma_f32 v176, v159, v163, v162
	v_fma_f32 v164, |v176|, s16, v117
	v_fma_f32 v165, |v176|, s17, v118
	v_fma_f32 v166, |v176|, s18, v119
	v_lshrrev_b32_e32 v167, 26, v176
	v_min3_u32 v164, v164, v165, v166
	v_bfi_b32 v168, 31, v164, v167
	s_nop 1
	v_mul_u32_u24_dpp v170, v168, v180 quad_perm:[1,2,3,3] row_mask:0xf bank_mask:0xf bound_ctrl:1
	v_mad_u32_u24 v171, v168, v181, v170
	ds_write_b8_d16_hi v184, v171 offset:544
	s_barrier
	global_store_short_d16_hi v185, v176, s[48:49]
	s_waitcnt lgkmcnt(0)
	s_barrier
	ds_read_b128 v[122:125], v192 offset:544
	ds_read_b64 v[126:127], v192 offset:560
	ds_read_b128 v[128:131], v192 offset:672
	ds_read_b64 v[132:133], v192 offset:688
	s_nop 7
	s_waitcnt lgkmcnt(2)
	v_mfma_f32_16x16x128_f8f6f4 v[134:137], v[122:127], v[2:7], 0 cbsz:2 blgp:2
	v_mfma_f32_16x16x128_f8f6f4 v[138:141], v[122:127], v[14:19], 0 cbsz:2 blgp:2
	v_mfma_f32_16x16x128_f8f6f4 v[142:145], v[122:127], v[26:31], v[188:191] cbsz:2 blgp:2
	v_mfma_f32_16x16x128_f8f6f4 v[204:207], v[122:127], v[38:43], 0 cbsz:2 blgp:2
	v_mfma_f32_16x16x128_f8f6f4 v[208:211], v[122:127], v[50:55], 0 cbsz:2 blgp:2
	v_mfma_f32_16x16x128_f8f6f4 v[212:215], v[122:127], v[62:67], v[188:191] cbsz:2 blgp:2
	s_waitcnt lgkmcnt(0)
	v_mfma_f32_16x16x128_f8f6f4 v[134:137], v[128:133], v[8:13], v[134:137] cbsz:2 blgp:2
	v_mfma_f32_16x16x128_f8f6f4 v[204:207], v[128:133], v[44:49], v[204:207] cbsz:2 blgp:2
	v_mfma_f32_16x16x128_f8f6f4 v[138:141], v[128:133], v[20:25], v[138:141] cbsz:2 blgp:2
	v_mfma_f32_16x16x128_f8f6f4 v[208:211], v[128:133], v[56:61], v[208:211] cbsz:2 blgp:2
	v_mfma_f32_16x16x128_f8f6f4 v[142:145], v[128:133], v[32:37], v[142:145] cbsz:2 blgp:2
	v_mfma_f32_16x16x128_f8f6f4 v[212:215], v[128:133], v[68:73], v[212:215] cbsz:2 blgp:2
	v_cndmask_b32_e64 v158, v134, v204, s[4:5]
	v_cndmask_b32_e64 v159, v138, v208, s[4:5]
	v_fma_mix_f32 v158, v158, v1, v148 op_sel:[0,0,1] op_sel_hi:[0,0,1]
	v_fma_mix_f32 v159, v159, v99, v152 op_sel:[0,0,1] op_sel_hi:[0,0,1]
	v_exp_f32_e32 v158, v158
	v_exp_f32_e32 v159, v159
	v_fma_f32 v158, v158, v186, v186
	v_add_f32_e32 v159, 1.0, v159
	v_rcp_f32_e32 v158, v158
	v_rcp_f32_e32 v159, v159
	v_cndmask_b32_e64 v160, v142, v212, s[4:5]
	v_fma_mix_f32 v161, v158, v160, v156 op_sel:[0,0,1] op_sel_hi:[0,0,1]
	v_exp_f32_e32 v161, v161
	s_add_u32 s48, s48, s40
	v_add_f32_e32 v161, 1.0, v161
	v_rcp_f32_e32 v161, v161
	s_addc_u32 s49, s49, s41
	v_fma_f32 v162, v161, -2.0, 1.0
	v_sub_f32_e32 v163, v176, v162
	v_fma_f32 v176, v159, v163, v162
	v_fma_f32 v164, |v176|, s16, v117
	v_fma_f32 v165, |v176|, s17, v118
	v_fma_f32 v166, |v176|, s18, v119
	v_lshrrev_b32_e32 v167, 26, v176
	v_min3_u32 v164, v164, v165, v166
	v_bfi_b32 v168, 31, v164, v167
	s_nop 1
	v_mul_u32_u24_dpp v170, v168, v180 quad_perm:[1,2,3,3] row_mask:0xf bank_mask:0xf bound_ctrl:1
	v_mad_u32_u24 v171, v168, v181, v170
	ds_write_b8_d16_hi v184, v171
	s_barrier
	global_store_short_d16_hi v185, v176, s[48:49]
	s_waitcnt lgkmcnt(0)
	s_barrier
	ds_read_b128 v[122:125], v192 offset:0
	ds_read_b64 v[126:127], v192 offset:16
	ds_read_b128 v[128:131], v192 offset:128
	ds_read_b64 v[132:133], v192 offset:144
	s_nop 7
	s_waitcnt lgkmcnt(2)
	v_mfma_f32_16x16x128_f8f6f4 v[134:137], v[122:127], v[2:7], 0 cbsz:2 blgp:2
	v_mfma_f32_16x16x128_f8f6f4 v[138:141], v[122:127], v[14:19], 0 cbsz:2 blgp:2
	v_mfma_f32_16x16x128_f8f6f4 v[142:145], v[122:127], v[26:31], v[188:191] cbsz:2 blgp:2
	v_mfma_f32_16x16x128_f8f6f4 v[204:207], v[122:127], v[38:43], 0 cbsz:2 blgp:2
	v_mfma_f32_16x16x128_f8f6f4 v[208:211], v[122:127], v[50:55], 0 cbsz:2 blgp:2
	v_mfma_f32_16x16x128_f8f6f4 v[212:215], v[122:127], v[62:67], v[188:191] cbsz:2 blgp:2
	s_waitcnt lgkmcnt(0)
	v_mfma_f32_16x16x128_f8f6f4 v[134:137], v[128:133], v[8:13], v[134:137] cbsz:2 blgp:2
	v_mfma_f32_16x16x128_f8f6f4 v[204:207], v[128:133], v[44:49], v[204:207] cbsz:2 blgp:2
	v_mfma_f32_16x16x128_f8f6f4 v[138:141], v[128:133], v[20:25], v[138:141] cbsz:2 blgp:2
	v_mfma_f32_16x16x128_f8f6f4 v[208:211], v[128:133], v[56:61], v[208:211] cbsz:2 blgp:2
	v_mfma_f32_16x16x128_f8f6f4 v[142:145], v[128:133], v[32:37], v[142:145] cbsz:2 blgp:2
	v_mfma_f32_16x16x128_f8f6f4 v[212:215], v[128:133], v[68:73], v[212:215] cbsz:2 blgp:2
	v_cndmask_b32_e64 v158, v134, v204, s[4:5]
	v_cndmask_b32_e64 v159, v138, v208, s[4:5]
	v_fma_mix_f32 v158, v158, v1, v149 op_sel_hi:[0,0,1]
	v_fma_mix_f32 v159, v159, v99, v153 op_sel_hi:[0,0,1]
	v_exp_f32_e32 v158, v158
	v_exp_f32_e32 v159, v159
	v_fma_f32 v158, v158, v186, v186
	v_add_f32_e32 v159, 1.0, v159
	v_rcp_f32_e32 v158, v158
	v_rcp_f32_e32 v159, v159
	v_cndmask_b32_e64 v160, v142, v212, s[4:5]
	v_fma_mix_f32 v161, v158, v160, v157 op_sel_hi:[0,0,1]
	v_exp_f32_e32 v161, v161
	s_add_u32 s48, s48, s40
	v_add_f32_e32 v161, 1.0, v161
	v_rcp_f32_e32 v161, v161
	s_addc_u32 s49, s49, s41
	v_fma_f32 v162, v161, -2.0, 1.0
	v_sub_f32_e32 v163, v176, v162
	v_fma_f32 v176, v159, v163, v162
	v_fma_f32 v164, |v176|, s16, v117
	v_fma_f32 v165, |v176|, s17, v118
	v_fma_f32 v166, |v176|, s18, v119
	v_lshrrev_b32_e32 v167, 26, v176
	v_min3_u32 v164, v164, v165, v166
	v_bfi_b32 v168, 31, v164, v167
	s_nop 1
	v_mul_u32_u24_dpp v170, v168, v180 quad_perm:[1,2,3,3] row_mask:0xf bank_mask:0xf bound_ctrl:1
	v_mad_u32_u24 v171, v168, v181, v170
	ds_write_b8_d16_hi v184, v171 offset:544
	s_barrier
	global_store_short_d16_hi v185, v176, s[48:49]
	s_waitcnt lgkmcnt(0)
	s_barrier
	ds_read_b128 v[122:125], v192 offset:544
	ds_read_b64 v[126:127], v192 offset:560
	ds_read_b128 v[128:131], v192 offset:672
	ds_read_b64 v[132:133], v192 offset:688
	s_add_i32 s44, s44, 16
	s_nop 7
	s_waitcnt lgkmcnt(2)
	v_mfma_f32_16x16x128_f8f6f4 v[134:137], v[122:127], v[2:7], 0 cbsz:2 blgp:2
	v_mfma_f32_16x16x128_f8f6f4 v[138:141], v[122:127], v[14:19], 0 cbsz:2 blgp:2
	v_mfma_f32_16x16x128_f8f6f4 v[142:145], v[122:127], v[26:31], v[188:191] cbsz:2 blgp:2
	v_mfma_f32_16x16x128_f8f6f4 v[204:207], v[122:127], v[38:43], 0 cbsz:2 blgp:2
	v_mfma_f32_16x16x128_f8f6f4 v[208:211], v[122:127], v[50:55], 0 cbsz:2 blgp:2
	v_mfma_f32_16x16x128_f8f6f4 v[212:215], v[122:127], v[62:67], v[188:191] cbsz:2 blgp:2
	s_waitcnt lgkmcnt(0)
	v_mfma_f32_16x16x128_f8f6f4 v[134:137], v[128:133], v[8:13], v[134:137] cbsz:2 blgp:2
	v_mfma_f32_16x16x128_f8f6f4 v[204:207], v[128:133], v[44:49], v[204:207] cbsz:2 blgp:2
	v_mfma_f32_16x16x128_f8f6f4 v[138:141], v[128:133], v[20:25], v[138:141] cbsz:2 blgp:2
	v_mfma_f32_16x16x128_f8f6f4 v[208:211], v[128:133], v[56:61], v[208:211] cbsz:2 blgp:2
	v_mfma_f32_16x16x128_f8f6f4 v[142:145], v[128:133], v[32:37], v[142:145] cbsz:2 blgp:2
	v_mfma_f32_16x16x128_f8f6f4 v[212:215], v[128:133], v[68:73], v[212:215] cbsz:2 blgp:2
	v_cndmask_b32_e64 v158, v134, v204, s[4:5]
	v_cndmask_b32_e64 v159, v138, v208, s[4:5]
	v_fma_mix_f32 v158, v158, v1, v149 op_sel:[0,0,1] op_sel_hi:[0,0,1]
	v_fma_mix_f32 v159, v159, v99, v153 op_sel:[0,0,1] op_sel_hi:[0,0,1]
	v_exp_f32_e32 v158, v158
	v_exp_f32_e32 v159, v159
	v_fma_f32 v158, v158, v186, v186
	v_add_f32_e32 v159, 1.0, v159
	v_rcp_f32_e32 v158, v158
	v_rcp_f32_e32 v159, v159
	v_cndmask_b32_e64 v160, v142, v212, s[4:5]
	v_fma_mix_f32 v161, v158, v160, v157 op_sel:[0,0,1] op_sel_hi:[0,0,1]
	v_exp_f32_e32 v161, v161
	s_add_u32 s48, s48, s40
	v_add_f32_e32 v161, 1.0, v161
	v_rcp_f32_e32 v161, v161
	s_addc_u32 s49, s49, s41
	v_fma_f32 v162, v161, -2.0, 1.0
	v_sub_f32_e32 v163, v176, v162
	v_fma_f32 v176, v159, v163, v162
	v_fma_f32 v164, |v176|, s16, v117
	v_fma_f32 v165, |v176|, s17, v118
	v_fma_f32 v166, |v176|, s18, v119
	v_lshrrev_b32_e32 v167, 26, v176
	v_min3_u32 v164, v164, v165, v166
	v_bfi_b32 v168, 31, v164, v167
	s_nop 1
	v_mul_u32_u24_dpp v170, v168, v180 quad_perm:[1,2,3,3] row_mask:0xf bank_mask:0xf bound_ctrl:1
	v_mad_u32_u24 v171, v168, v181, v170
	ds_write_b8_d16_hi v184, v171
	s_barrier
	global_store_short_d16_hi v185, v176, s[48:49]
	s_cmp_lt_i32 s44, s45
	s_cbranch_scc1 .Lscan_loop_b_st
	s_waitcnt lgkmcnt(0)
	s_barrier

.Lscan_enter_b_f2:
	ds_read_b128 v[122:125], v192 offset:0
	ds_read_b64 v[126:127], v192 offset:16
	ds_read_b128 v[128:131], v192 offset:128
	ds_read_b64 v[132:133], v192 offset:144
	s_waitcnt vmcnt(8)
	global_load_dwordx4 v[146:149], v[196:197], off
	global_load_dwordx4 v[150:153], v[196:197], off offset:512
	global_load_dwordx4 v[154:157], v[196:197], off offset:1024
	v_lshl_add_u64 v[196:197], v[196:197], 0, s[42:43]
	s_nop 7
	s_waitcnt lgkmcnt(2)
	v_mfma_f32_16x16x128_f8f6f4 v[134:137], v[122:127], v[2:7], 0 cbsz:2 blgp:2
	v_mfma_f32_16x16x128_f8f6f4 v[138:141], v[122:127], v[14:19], 0 cbsz:2 blgp:2
	v_mfma_f32_16x16x128_f8f6f4 v[142:145], v[122:127], v[26:31], v[188:191] cbsz:2 blgp:2
	v_mfma_f32_16x16x128_f8f6f4 v[204:207], v[122:127], v[38:43], 0 cbsz:2 blgp:2
	v_mfma_f32_16x16x128_f8f6f4 v[208:211], v[122:127], v[50:55], 0 cbsz:2 blgp:2
	v_mfma_f32_16x16x128_f8f6f4 v[212:215], v[122:127], v[62:67], v[188:191] cbsz:2 blgp:2
	s_waitcnt lgkmcnt(0)
	v_mfma_f32_16x16x128_f8f6f4 v[134:137], v[128:133], v[8:13], v[134:137] cbsz:2 blgp:2
	v_mfma_f32_16x16x128_f8f6f4 v[204:207], v[128:133], v[44:49], v[204:207] cbsz:2 blgp:2
	v_mfma_f32_16x16x128_f8f6f4 v[138:141], v[128:133], v[20:25], v[138:141] cbsz:2 blgp:2
	v_mfma_f32_16x16x128_f8f6f4 v[208:211], v[128:133], v[56:61], v[208:211] cbsz:2 blgp:2
	v_mfma_f32_16x16x128_f8f6f4 v[142:145], v[128:133], v[32:37], v[142:145] cbsz:2 blgp:2
	v_mfma_f32_16x16x128_f8f6f4 v[212:215], v[128:133], v[68:73], v[212:215] cbsz:2 blgp:2
	v_cndmask_b32_e64 v158, v134, v204, s[0:1]
	v_cndmask_b32_e64 v159, v138, v208, s[0:1]
	v_fma_mix_f32 v158, v158, v100, v82 op_sel_hi:[0,0,1]
	v_fma_mix_f32 v159, v159, v101, v74 op_sel_hi:[0,0,1]
	v_exp_f32_e32 v158, v158
	v_exp_f32_e32 v159, v159
	v_fma_f32 v158, v158, v186, v186
	v_add_f32_e32 v159, 1.0, v159
	v_rcp_f32_e32 v158, v158
	v_rcp_f32_e32 v159, v159
	v_cndmask_b32_e64 v160, v142, v212, s[0:1]
	v_fma_mix_f32 v161, v158, v160, v78 op_sel_hi:[0,0,1]
	v_exp_f32_e32 v161, v161
	s_add_u32 s48, s48, s40
	v_add_f32_e32 v161, 1.0, v161
	v_rcp_f32_e32 v161, v161
	s_addc_u32 s49, s49, s41
	v_fma_f32 v162, v161, -2.0, 1.0
	v_sub_f32_e32 v163, v176, v162
	v_fma_f32 v176, v159, v163, v162
	v_fma_f32 v164, |v176|, s17, v113
	v_fma_f32 v165, |v176|, s18, v114
	v_fma_f32 v166, |v176|, s19, v115
	v_lshrrev_b32_e32 v167, 26, v176
	v_min3_u32 v164, v164, v165, v166
	v_bfi_b32 v168, 31, v164, v167
	s_nop 1
	v_mul_u32_u24_dpp v170, v168, v180 quad_perm:[1,2,3,3] row_mask:0xf bank_mask:0xf bound_ctrl:1
	v_mad_u32_u24 v171, v168, v181, v170
	ds_write_b8_d16_hi v184, v171 offset:544
	s_barrier
	global_store_short_d16_hi v185, v176, s[48:49]
	s_waitcnt lgkmcnt(0)
	s_barrier
	ds_read_b128 v[122:125], v192 offset:544
	ds_read_b64 v[126:127], v192 offset:560
	ds_read_b128 v[128:131], v192 offset:672
	ds_read_b64 v[132:133], v192 offset:688
	s_nop 7
	s_waitcnt lgkmcnt(2)
	v_mfma_f32_16x16x128_f8f6f4 v[134:137], v[122:127], v[2:7], 0 cbsz:2 blgp:2
	v_mfma_f32_16x16x128_f8f6f4 v[138:141], v[122:127], v[14:19], 0 cbsz:2 blgp:2
	v_mfma_f32_16x16x128_f8f6f4 v[142:145], v[122:127], v[26:31], v[188:191] cbsz:2 blgp:2
	v_mfma_f32_16x16x128_f8f6f4 v[204:207], v[122:127], v[38:43], 0 cbsz:2 blgp:2
	v_mfma_f32_16x16x128_f8f6f4 v[208:211], v[122:127], v[50:55], 0 cbsz:2 blgp:2
	v_mfma_f32_16x16x128_f8f6f4 v[212:215], v[122:127], v[62:67], v[188:191] cbsz:2 blgp:2
	s_waitcnt lgkmcnt(0)
	v_mfma_f32_16x16x128_f8f6f4 v[134:137], v[128:133], v[8:13], v[134:137] cbsz:2 blgp:2
	v_mfma_f32_16x16x128_f8f6f4 v[204:207], v[128:133], v[44:49], v[204:207] cbsz:2 blgp:2
	v_mfma_f32_16x16x128_f8f6f4 v[138:141], v[128:133], v[20:25], v[138:141] cbsz:2 blgp:2
	v_mfma_f32_16x16x128_f8f6f4 v[208:211], v[128:133], v[56:61], v[208:211] cbsz:2 blgp:2
	v_mfma_f32_16x16x128_f8f6f4 v[142:145], v[128:133], v[32:37], v[142:145] cbsz:2 blgp:2
	v_mfma_f32_16x16x128_f8f6f4 v[212:215], v[128:133], v[68:73], v[212:215] cbsz:2 blgp:2
	v_cndmask_b32_e64 v158, v134, v204, s[0:1]
	v_cndmask_b32_e64 v159, v138, v208, s[0:1]
	v_fma_mix_f32 v158, v158, v100, v82 op_sel:[0,0,1] op_sel_hi:[0,0,1]
	v_fma_mix_f32 v159, v159, v101, v74 op_sel:[0,0,1] op_sel_hi:[0,0,1]
	v_exp_f32_e32 v158, v158
	v_exp_f32_e32 v159, v159
	v_fma_f32 v158, v158, v186, v186
	v_add_f32_e32 v159, 1.0, v159
	v_rcp_f32_e32 v158, v158
	v_rcp_f32_e32 v159, v159
	v_cndmask_b32_e64 v160, v142, v212, s[0:1]
	v_fma_mix_f32 v161, v158, v160, v78 op_sel:[0,0,1] op_sel_hi:[0,0,1]
	v_exp_f32_e32 v161, v161
	s_add_u32 s48, s48, s40
	v_add_f32_e32 v161, 1.0, v161
	v_rcp_f32_e32 v161, v161
	s_addc_u32 s49, s49, s41
	v_fma_f32 v162, v161, -2.0, 1.0
	v_sub_f32_e32 v163, v176, v162
	v_fma_f32 v176, v159, v163, v162
	v_fma_f32 v164, |v176|, s17, v113
	v_fma_f32 v165, |v176|, s18, v114
	v_fma_f32 v166, |v176|, s19, v115
	v_lshrrev_b32_e32 v167, 26, v176
	v_min3_u32 v164, v164, v165, v166
	v_bfi_b32 v168, 31, v164, v167
	s_nop 1
	v_mul_u32_u24_dpp v170, v168, v180 quad_perm:[1,2,3,3] row_mask:0xf bank_mask:0xf bound_ctrl:1
	v_mad_u32_u24 v171, v168, v181, v170
	ds_write_b8_d16_hi v184, v171
	s_barrier
	global_store_short_d16_hi v185, v176, s[48:49]
	s_waitcnt lgkmcnt(0)
	s_barrier
	ds_read_b128 v[122:125], v192 offset:0
	ds_read_b64 v[126:127], v192 offset:16
	ds_read_b128 v[128:131], v192 offset:128
	ds_read_b64 v[132:133], v192 offset:144
	s_nop 7
	s_waitcnt lgkmcnt(2)
	v_mfma_f32_16x16x128_f8f6f4 v[134:137], v[122:127], v[2:7], 0 cbsz:2 blgp:2
	v_mfma_f32_16x16x128_f8f6f4 v[138:141], v[122:127], v[14:19], 0 cbsz:2 blgp:2
	v_mfma_f32_16x16x128_f8f6f4 v[142:145], v[122:127], v[26:31], v[188:191] cbsz:2 blgp:2
	v_mfma_f32_16x16x128_f8f6f4 v[204:207], v[122:127], v[38:43], 0 cbsz:2 blgp:2
	v_mfma_f32_16x16x128_f8f6f4 v[208:211], v[122:127], v[50:55], 0 cbsz:2 blgp:2
	v_mfma_f32_16x16x128_f8f6f4 v[212:215], v[122:127], v[62:67], v[188:191] cbsz:2 blgp:2
	s_waitcnt lgkmcnt(0)
	v_mfma_f32_16x16x128_f8f6f4 v[134:137], v[128:133], v[8:13], v[134:137] cbsz:2 blgp:2
	v_mfma_f32_16x16x128_f8f6f4 v[204:207], v[128:133], v[44:49], v[204:207] cbsz:2 blgp:2
	v_mfma_f32_16x16x128_f8f6f4 v[138:141], v[128:133], v[20:25], v[138:141] cbsz:2 blgp:2
	v_mfma_f32_16x16x128_f8f6f4 v[208:211], v[128:133], v[56:61], v[208:211] cbsz:2 blgp:2
	v_mfma_f32_16x16x128_f8f6f4 v[142:145], v[128:133], v[32:37], v[142:145] cbsz:2 blgp:2
	v_mfma_f32_16x16x128_f8f6f4 v[212:215], v[128:133], v[68:73], v[212:215] cbsz:2 blgp:2
	v_cndmask_b32_e64 v158, v134, v204, s[0:1]
	v_cndmask_b32_e64 v159, v138, v208, s[0:1]
	v_fma_mix_f32 v158, v158, v100, v83 op_sel_hi:[0,0,1]
	v_fma_mix_f32 v159, v159, v101, v75 op_sel_hi:[0,0,1]
	v_exp_f32_e32 v158, v158
	v_exp_f32_e32 v159, v159
	v_fma_f32 v158, v158, v186, v186
	v_add_f32_e32 v159, 1.0, v159
	v_rcp_f32_e32 v158, v158
	v_rcp_f32_e32 v159, v159
	v_cndmask_b32_e64 v160, v142, v212, s[0:1]
	v_fma_mix_f32 v161, v158, v160, v79 op_sel_hi:[0,0,1]
	v_exp_f32_e32 v161, v161
	s_add_u32 s48, s48, s40
	v_add_f32_e32 v161, 1.0, v161
	v_rcp_f32_e32 v161, v161
	s_addc_u32 s49, s49, s41
	v_fma_f32 v162, v161, -2.0, 1.0
	v_sub_f32_e32 v163, v176, v162
	v_fma_f32 v176, v159, v163, v162
	v_fma_f32 v164, |v176|, s17, v113
	v_fma_f32 v165, |v176|, s18, v114
	v_fma_f32 v166, |v176|, s19, v115
	v_lshrrev_b32_e32 v167, 26, v176
	v_min3_u32 v164, v164, v165, v166
	v_bfi_b32 v168, 31, v164, v167
	s_nop 1
	v_mul_u32_u24_dpp v170, v168, v180 quad_perm:[1,2,3,3] row_mask:0xf bank_mask:0xf bound_ctrl:1
	v_mad_u32_u24 v171, v168, v181, v170
	ds_write_b8_d16_hi v184, v171 offset:544
	s_barrier
	global_store_short_d16_hi v185, v176, s[48:49]
	s_waitcnt lgkmcnt(0)
	s_barrier
	ds_read_b128 v[122:125], v192 offset:544
	ds_read_b64 v[126:127], v192 offset:560
	ds_read_b128 v[128:131], v192 offset:672
	ds_read_b64 v[132:133], v192 offset:688
	s_nop 7
	s_waitcnt lgkmcnt(2)
	v_mfma_f32_16x16x128_f8f6f4 v[134:137], v[122:127], v[2:7], 0 cbsz:2 blgp:2
	v_mfma_f32_16x16x128_f8f6f4 v[138:141], v[122:127], v[14:19], 0 cbsz:2 blgp:2
	v_mfma_f32_16x16x128_f8f6f4 v[142:145], v[122:127], v[26:31], v[188:191] cbsz:2 blgp:2
	v_mfma_f32_16x16x128_f8f6f4 v[204:207], v[122:127], v[38:43], 0 cbsz:2 blgp:2
	v_mfma_f32_16x16x128_f8f6f4 v[208:211], v[122:127], v[50:55], 0 cbsz:2 blgp:2
	v_mfma_f32_16x16x128_f8f6f4 v[212:215], v[122:127], v[62:67], v[188:191] cbsz:2 blgp:2
	s_waitcnt lgkmcnt(0)
	v_mfma_f32_16x16x128_f8f6f4 v[134:137], v[128:133], v[8:13], v[134:137] cbsz:2 blgp:2
	v_mfma_f32_16x16x128_f8f6f4 v[204:207], v[128:133], v[44:49], v[204:207] cbsz:2 blgp:2
	v_mfma_f32_16x16x128_f8f6f4 v[138:141], v[128:133], v[20:25], v[138:141] cbsz:2 blgp:2
	v_mfma_f32_16x16x128_f8f6f4 v[208:211], v[128:133], v[56:61], v[208:211] cbsz:2 blgp:2
	v_mfma_f32_16x16x128_f8f6f4 v[142:145], v[128:133], v[32:37], v[142:145] cbsz:2 blgp:2
	v_mfma_f32_16x16x128_f8f6f4 v[212:215], v[128:133], v[68:73], v[212:215] cbsz:2 blgp:2
	v_cndmask_b32_e64 v158, v134, v204, s[0:1]
	v_cndmask_b32_e64 v159, v138, v208, s[0:1]
	v_fma_mix_f32 v158, v158, v100, v83 op_sel:[0,0,1] op_sel_hi:[0,0,1]
	v_fma_mix_f32 v159, v159, v101, v75 op_sel:[0,0,1] op_sel_hi:[0,0,1]
	v_exp_f32_e32 v158, v158
	v_exp_f32_e32 v159, v159
	v_fma_f32 v158, v158, v186, v186
	v_add_f32_e32 v159, 1.0, v159
	v_rcp_f32_e32 v158, v158
	v_rcp_f32_e32 v159, v159
	v_cndmask_b32_e64 v160, v142, v212, s[0:1]
	v_fma_mix_f32 v161, v158, v160, v79 op_sel:[0,0,1] op_sel_hi:[0,0,1]
	v_exp_f32_e32 v161, v161
	s_add_u32 s48, s48, s40
	v_add_f32_e32 v161, 1.0, v161
	v_rcp_f32_e32 v161, v161
	s_addc_u32 s49, s49, s41
	v_fma_f32 v162, v161, -2.0, 1.0
	v_sub_f32_e32 v163, v176, v162
	v_fma_f32 v176, v159, v163, v162
	v_fma_f32 v164, |v176|, s17, v113
	v_fma_f32 v165, |v176|, s18, v114
	v_fma_f32 v166, |v176|, s19, v115
	v_lshrrev_b32_e32 v167, 26, v176
	v_min3_u32 v164, v164, v165, v166
	v_bfi_b32 v168, 31, v164, v167
	s_nop 1
	v_mul_u32_u24_dpp v170, v168, v180 quad_perm:[1,2,3,3] row_mask:0xf bank_mask:0xf bound_ctrl:1
	v_mad_u32_u24 v171, v168, v181, v170
	ds_write_b8_d16_hi v184, v171
	s_barrier
	global_store_short_d16_hi v185, v176, s[48:49]
	s_waitcnt lgkmcnt(0)
	s_barrier
	ds_read_b128 v[122:125], v192 offset:0
	ds_read_b64 v[126:127], v192 offset:16
	ds_read_b128 v[128:131], v192 offset:128
	ds_read_b64 v[132:133], v192 offset:144
	s_nop 7
	s_waitcnt lgkmcnt(2)
	v_mfma_f32_16x16x128_f8f6f4 v[134:137], v[122:127], v[2:7], 0 cbsz:2 blgp:2
	v_mfma_f32_16x16x128_f8f6f4 v[138:141], v[122:127], v[14:19], 0 cbsz:2 blgp:2
	v_mfma_f32_16x16x128_f8f6f4 v[142:145], v[122:127], v[26:31], v[188:191] cbsz:2 blgp:2
	v_mfma_f32_16x16x128_f8f6f4 v[204:207], v[122:127], v[38:43], 0 cbsz:2 blgp:2
	v_mfma_f32_16x16x128_f8f6f4 v[208:211], v[122:127], v[50:55], 0 cbsz:2 blgp:2
	v_mfma_f32_16x16x128_f8f6f4 v[212:215], v[122:127], v[62:67], v[188:191] cbsz:2 blgp:2
	s_waitcnt lgkmcnt(0)
	v_mfma_f32_16x16x128_f8f6f4 v[134:137], v[128:133], v[8:13], v[134:137] cbsz:2 blgp:2
	v_mfma_f32_16x16x128_f8f6f4 v[204:207], v[128:133], v[44:49], v[204:207] cbsz:2 blgp:2
	v_mfma_f32_16x16x128_f8f6f4 v[138:141], v[128:133], v[20:25], v[138:141] cbsz:2 blgp:2
	v_mfma_f32_16x16x128_f8f6f4 v[208:211], v[128:133], v[56:61], v[208:211] cbsz:2 blgp:2
	v_mfma_f32_16x16x128_f8f6f4 v[142:145], v[128:133], v[32:37], v[142:145] cbsz:2 blgp:2
	v_mfma_f32_16x16x128_f8f6f4 v[212:215], v[128:133], v[68:73], v[212:215] cbsz:2 blgp:2
	v_cndmask_b32_e64 v158, v134, v204, s[0:1]
	v_cndmask_b32_e64 v159, v138, v208, s[0:1]
	v_fma_mix_f32 v158, v158, v100, v84 op_sel_hi:[0,0,1]
	v_fma_mix_f32 v159, v159, v101, v76 op_sel_hi:[0,0,1]
	v_exp_f32_e32 v158, v158
	v_exp_f32_e32 v159, v159
	v_fma_f32 v158, v158, v186, v186
	v_add_f32_e32 v159, 1.0, v159
	v_rcp_f32_e32 v158, v158
	v_rcp_f32_e32 v159, v159
	v_cndmask_b32_e64 v160, v142, v212, s[0:1]
	v_fma_mix_f32 v161, v158, v160, v80 op_sel_hi:[0,0,1]
	v_exp_f32_e32 v161, v161
	s_add_u32 s48, s48, s40
	v_add_f32_e32 v161, 1.0, v161
	v_rcp_f32_e32 v161, v161
	s_addc_u32 s49, s49, s41
	v_fma_f32 v162, v161, -2.0, 1.0
	v_sub_f32_e32 v163, v176, v162
	v_fma_f32 v176, v159, v163, v162
	v_fma_f32 v164, |v176|, s17, v113
	v_fma_f32 v165, |v176|, s18, v114
	v_fma_f32 v166, |v176|, s19, v115
	v_lshrrev_b32_e32 v167, 26, v176
	v_min3_u32 v164, v164, v165, v166
	v_bfi_b32 v168, 31, v164, v167
	s_nop 1
	v_mul_u32_u24_dpp v170, v168, v180 quad_perm:[1,2,3,3] row_mask:0xf bank_mask:0xf bound_ctrl:1
	v_mad_u32_u24 v171, v168, v181, v170
	ds_write_b8_d16_hi v184, v171 offset:544
	s_barrier
	global_store_short_d16_hi v185, v176, s[48:49]
	s_waitcnt lgkmcnt(0)
	s_barrier
	ds_read_b128 v[122:125], v192 offset:544
	ds_read_b64 v[126:127], v192 offset:560
	ds_read_b128 v[128:131], v192 offset:672
	ds_read_b64 v[132:133], v192 offset:688
	s_nop 7
	s_waitcnt lgkmcnt(2)
	v_mfma_f32_16x16x128_f8f6f4 v[134:137], v[122:127], v[2:7], 0 cbsz:2 blgp:2
	v_mfma_f32_16x16x128_f8f6f4 v[138:141], v[122:127], v[14:19], 0 cbsz:2 blgp:2
	v_mfma_f32_16x16x128_f8f6f4 v[142:145], v[122:127], v[26:31], v[188:191] cbsz:2 blgp:2
	v_mfma_f32_16x16x128_f8f6f4 v[204:207], v[122:127], v[38:43], 0 cbsz:2 blgp:2
	v_mfma_f32_16x16x128_f8f6f4 v[208:211], v[122:127], v[50:55], 0 cbsz:2 blgp:2
	v_mfma_f32_16x16x128_f8f6f4 v[212:215], v[122:127], v[62:67], v[188:191] cbsz:2 blgp:2
	s_waitcnt lgkmcnt(0)
	v_mfma_f32_16x16x128_f8f6f4 v[134:137], v[128:133], v[8:13], v[134:137] cbsz:2 blgp:2
	v_mfma_f32_16x16x128_f8f6f4 v[204:207], v[128:133], v[44:49], v[204:207] cbsz:2 blgp:2
	v_mfma_f32_16x16x128_f8f6f4 v[138:141], v[128:133], v[20:25], v[138:141] cbsz:2 blgp:2
	v_mfma_f32_16x16x128_f8f6f4 v[208:211], v[128:133], v[56:61], v[208:211] cbsz:2 blgp:2
	v_mfma_f32_16x16x128_f8f6f4 v[142:145], v[128:133], v[32:37], v[142:145] cbsz:2 blgp:2
	v_mfma_f32_16x16x128_f8f6f4 v[212:215], v[128:133], v[68:73], v[212:215] cbsz:2 blgp:2
	v_cndmask_b32_e64 v158, v134, v204, s[0:1]
	v_cndmask_b32_e64 v159, v138, v208, s[0:1]
	v_fma_mix_f32 v158, v158, v100, v84 op_sel:[0,0,1] op_sel_hi:[0,0,1]
	v_fma_mix_f32 v159, v159, v101, v76 op_sel:[0,0,1] op_sel_hi:[0,0,1]
	v_exp_f32_e32 v158, v158
	v_exp_f32_e32 v159, v159
	v_fma_f32 v158, v158, v186, v186
	v_add_f32_e32 v159, 1.0, v159
	v_rcp_f32_e32 v158, v158
	v_rcp_f32_e32 v159, v159
	v_cndmask_b32_e64 v160, v142, v212, s[0:1]
	v_fma_mix_f32 v161, v158, v160, v80 op_sel:[0,0,1] op_sel_hi:[0,0,1]
	v_exp_f32_e32 v161, v161
	s_add_u32 s48, s48, s40
	v_add_f32_e32 v161, 1.0, v161
	v_rcp_f32_e32 v161, v161
	s_addc_u32 s49, s49, s41
	v_fma_f32 v162, v161, -2.0, 1.0
	v_sub_f32_e32 v163, v176, v162
	v_fma_f32 v176, v159, v163, v162
	v_fma_f32 v164, |v176|, s17, v113
	v_fma_f32 v165, |v176|, s18, v114
	v_fma_f32 v166, |v176|, s19, v115
	v_lshrrev_b32_e32 v167, 26, v176
	v_min3_u32 v164, v164, v165, v166
	v_bfi_b32 v168, 31, v164, v167
	s_nop 1
	v_mul_u32_u24_dpp v170, v168, v180 quad_perm:[1,2,3,3] row_mask:0xf bank_mask:0xf bound_ctrl:1
	v_mad_u32_u24 v171, v168, v181, v170
	ds_write_b8_d16_hi v184, v171
	s_barrier
	global_store_short_d16_hi v185, v176, s[48:49]
	s_waitcnt lgkmcnt(0)
	s_barrier
	ds_read_b128 v[122:125], v192 offset:0
	ds_read_b64 v[126:127], v192 offset:16
	ds_read_b128 v[128:131], v192 offset:128
	ds_read_b64 v[132:133], v192 offset:144
	s_nop 7
	s_waitcnt lgkmcnt(2)
	v_mfma_f32_16x16x128_f8f6f4 v[134:137], v[122:127], v[2:7], 0 cbsz:2 blgp:2
	v_mfma_f32_16x16x128_f8f6f4 v[138:141], v[122:127], v[14:19], 0 cbsz:2 blgp:2
	v_mfma_f32_16x16x128_f8f6f4 v[142:145], v[122:127], v[26:31], v[188:191] cbsz:2 blgp:2
	v_mfma_f32_16x16x128_f8f6f4 v[204:207], v[122:127], v[38:43], 0 cbsz:2 blgp:2
	v_mfma_f32_16x16x128_f8f6f4 v[208:211], v[122:127], v[50:55], 0 cbsz:2 blgp:2
	v_mfma_f32_16x16x128_f8f6f4 v[212:215], v[122:127], v[62:67], v[188:191] cbsz:2 blgp:2
	s_waitcnt lgkmcnt(0)
	v_mfma_f32_16x16x128_f8f6f4 v[134:137], v[128:133], v[8:13], v[134:137] cbsz:2 blgp:2
	v_mfma_f32_16x16x128_f8f6f4 v[204:207], v[128:133], v[44:49], v[204:207] cbsz:2 blgp:2
	v_mfma_f32_16x16x128_f8f6f4 v[138:141], v[128:133], v[20:25], v[138:141] cbsz:2 blgp:2
	v_mfma_f32_16x16x128_f8f6f4 v[208:211], v[128:133], v[56:61], v[208:211] cbsz:2 blgp:2
	v_mfma_f32_16x16x128_f8f6f4 v[142:145], v[128:133], v[32:37], v[142:145] cbsz:2 blgp:2
	v_mfma_f32_16x16x128_f8f6f4 v[212:215], v[128:133], v[68:73], v[212:215] cbsz:2 blgp:2
	v_cndmask_b32_e64 v158, v134, v204, s[0:1]
	v_cndmask_b32_e64 v159, v138, v208, s[0:1]
	v_fma_mix_f32 v158, v158, v100, v85 op_sel_hi:[0,0,1]
	v_fma_mix_f32 v159, v159, v101, v77 op_sel_hi:[0,0,1]
	v_exp_f32_e32 v158, v158
	v_exp_f32_e32 v159, v159
	v_fma_f32 v158, v158, v186, v186
	v_add_f32_e32 v159, 1.0, v159
	v_rcp_f32_e32 v158, v158
	v_rcp_f32_e32 v159, v159
	v_cndmask_b32_e64 v160, v142, v212, s[0:1]
	v_fma_mix_f32 v161, v158, v160, v81 op_sel_hi:[0,0,1]
	v_exp_f32_e32 v161, v161
	s_add_u32 s48, s48, s40
	v_add_f32_e32 v161, 1.0, v161
	v_rcp_f32_e32 v161, v161
	s_addc_u32 s49, s49, s41
	v_fma_f32 v162, v161, -2.0, 1.0
	v_sub_f32_e32 v163, v176, v162
	v_fma_f32 v176, v159, v163, v162
	v_fma_f32 v164, |v176|, s17, v113
	v_fma_f32 v165, |v176|, s18, v114
	v_fma_f32 v166, |v176|, s19, v115
	v_lshrrev_b32_e32 v167, 26, v176
	v_min3_u32 v164, v164, v165, v166
	v_bfi_b32 v168, 31, v164, v167
	s_nop 1
	v_mul_u32_u24_dpp v170, v168, v180 quad_perm:[1,2,3,3] row_mask:0xf bank_mask:0xf bound_ctrl:1
	v_mad_u32_u24 v171, v168, v181, v170
	ds_write_b8_d16_hi v184, v171 offset:544
	s_barrier
	global_store_short_d16_hi v185, v176, s[48:49]
	s_waitcnt lgkmcnt(0)
	s_barrier
	ds_read_b128 v[122:125], v192 offset:544
	ds_read_b64 v[126:127], v192 offset:560
	ds_read_b128 v[128:131], v192 offset:672
	ds_read_b64 v[132:133], v192 offset:688
	s_nop 7
	s_waitcnt lgkmcnt(2)
	v_mfma_f32_16x16x128_f8f6f4 v[134:137], v[122:127], v[2:7], 0 cbsz:2 blgp:2
	v_mfma_f32_16x16x128_f8f6f4 v[138:141], v[122:127], v[14:19], 0 cbsz:2 blgp:2
	v_mfma_f32_16x16x128_f8f6f4 v[142:145], v[122:127], v[26:31], v[188:191] cbsz:2 blgp:2
	v_mfma_f32_16x16x128_f8f6f4 v[204:207], v[122:127], v[38:43], 0 cbsz:2 blgp:2
	v_mfma_f32_16x16x128_f8f6f4 v[208:211], v[122:127], v[50:55], 0 cbsz:2 blgp:2
	v_mfma_f32_16x16x128_f8f6f4 v[212:215], v[122:127], v[62:67], v[188:191] cbsz:2 blgp:2
	s_waitcnt lgkmcnt(0)
	v_mfma_f32_16x16x128_f8f6f4 v[134:137], v[128:133], v[8:13], v[134:137] cbsz:2 blgp:2
	v_mfma_f32_16x16x128_f8f6f4 v[204:207], v[128:133], v[44:49], v[204:207] cbsz:2 blgp:2
	v_mfma_f32_16x16x128_f8f6f4 v[138:141], v[128:133], v[20:25], v[138:141] cbsz:2 blgp:2
	v_mfma_f32_16x16x128_f8f6f4 v[208:211], v[128:133], v[56:61], v[208:211] cbsz:2 blgp:2
	v_mfma_f32_16x16x128_f8f6f4 v[142:145], v[128:133], v[32:37], v[142:145] cbsz:2 blgp:2
	v_mfma_f32_16x16x128_f8f6f4 v[212:215], v[128:133], v[68:73], v[212:215] cbsz:2 blgp:2
	v_cndmask_b32_e64 v158, v134, v204, s[0:1]
	v_cndmask_b32_e64 v159, v138, v208, s[0:1]
	v_fma_mix_f32 v158, v158, v100, v85 op_sel:[0,0,1] op_sel_hi:[0,0,1]
	v_fma_mix_f32 v159, v159, v101, v77 op_sel:[0,0,1] op_sel_hi:[0,0,1]
	v_exp_f32_e32 v158, v158
	v_exp_f32_e32 v159, v159
	v_fma_f32 v158, v158, v186, v186
	v_add_f32_e32 v159, 1.0, v159
	v_rcp_f32_e32 v158, v158
	v_rcp_f32_e32 v159, v159
	v_cndmask_b32_e64 v160, v142, v212, s[0:1]
	v_fma_mix_f32 v161, v158, v160, v81 op_sel:[0,0,1] op_sel_hi:[0,0,1]
	v_exp_f32_e32 v161, v161
	s_add_u32 s48, s48, s40
	v_add_f32_e32 v161, 1.0, v161
	v_rcp_f32_e32 v161, v161
	s_addc_u32 s49, s49, s41
	v_fma_f32 v162, v161, -2.0, 1.0
	v_sub_f32_e32 v163, v176, v162
	v_fma_f32 v176, v159, v163, v162
	v_fma_f32 v164, |v176|, s17, v113
	v_fma_f32 v165, |v176|, s18, v114
	v_fma_f32 v166, |v176|, s19, v115
	v_lshrrev_b32_e32 v167, 26, v176
	v_min3_u32 v164, v164, v165, v166
	v_bfi_b32 v168, 31, v164, v167
	s_nop 1
	v_mul_u32_u24_dpp v170, v168, v180 quad_perm:[1,2,3,3] row_mask:0xf bank_mask:0xf bound_ctrl:1
	v_mad_u32_u24 v171, v168, v181, v170
	ds_write_b8_d16_hi v184, v171
	s_barrier
	global_store_short_d16_hi v185, v176, s[48:49]
	s_waitcnt lgkmcnt(0)
	s_barrier
	ds_read_b128 v[122:125], v192 offset:0
	ds_read_b64 v[126:127], v192 offset:16
	ds_read_b128 v[128:131], v192 offset:128
	ds_read_b64 v[132:133], v192 offset:144
	s_waitcnt vmcnt(8)
	global_load_dwordx4 v[82:85], v[196:197], off
	global_load_dwordx4 v[74:77], v[196:197], off offset:512
	global_load_dwordx4 v[78:81], v[196:197], off offset:1024
	v_lshl_add_u64 v[196:197], v[196:197], 0, s[42:43]
	s_nop 7
	s_waitcnt lgkmcnt(2)
	v_mfma_f32_16x16x128_f8f6f4 v[134:137], v[122:127], v[2:7], 0 cbsz:2 blgp:2
	v_mfma_f32_16x16x128_f8f6f4 v[138:141], v[122:127], v[14:19], 0 cbsz:2 blgp:2
	v_mfma_f32_16x16x128_f8f6f4 v[142:145], v[122:127], v[26:31], v[188:191] cbsz:2 blgp:2
	v_mfma_f32_16x16x128_f8f6f4 v[204:207], v[122:127], v[38:43], 0 cbsz:2 blgp:2
	v_mfma_f32_16x16x128_f8f6f4 v[208:211], v[122:127], v[50:55], 0 cbsz:2 blgp:2
	v_mfma_f32_16x16x128_f8f6f4 v[212:215], v[122:127], v[62:67], v[188:191] cbsz:2 blgp:2
	s_waitcnt lgkmcnt(0)
	v_mfma_f32_16x16x128_f8f6f4 v[134:137], v[128:133], v[8:13], v[134:137] cbsz:2 blgp:2
	v_mfma_f32_16x16x128_f8f6f4 v[204:207], v[128:133], v[44:49], v[204:207] cbsz:2 blgp:2
	v_mfma_f32_16x16x128_f8f6f4 v[138:141], v[128:133], v[20:25], v[138:141] cbsz:2 blgp:2
	v_mfma_f32_16x16x128_f8f6f4 v[208:211], v[128:133], v[56:61], v[208:211] cbsz:2 blgp:2
	v_mfma_f32_16x16x128_f8f6f4 v[142:145], v[128:133], v[32:37], v[142:145] cbsz:2 blgp:2
	v_mfma_f32_16x16x128_f8f6f4 v[212:215], v[128:133], v[68:73], v[212:215] cbsz:2 blgp:2
	v_cndmask_b32_e64 v158, v134, v204, s[0:1]
	v_cndmask_b32_e64 v159, v138, v208, s[0:1]
	v_fma_mix_f32 v158, v158, v100, v146 op_sel_hi:[0,0,1]
	v_fma_mix_f32 v159, v159, v101, v150 op_sel_hi:[0,0,1]
	v_exp_f32_e32 v158, v158
	v_exp_f32_e32 v159, v159
	v_fma_f32 v158, v158, v186, v186
	v_add_f32_e32 v159, 1.0, v159
	v_rcp_f32_e32 v158, v158
	v_rcp_f32_e32 v159, v159
	v_cndmask_b32_e64 v160, v142, v212, s[0:1]
	v_fma_mix_f32 v161, v158, v160, v154 op_sel_hi:[0,0,1]
	v_exp_f32_e32 v161, v161
	s_add_u32 s48, s48, s40
	v_add_f32_e32 v161, 1.0, v161
	v_rcp_f32_e32 v161, v161
	s_addc_u32 s49, s49, s41
	v_fma_f32 v162, v161, -2.0, 1.0
	v_sub_f32_e32 v163, v176, v162
	v_fma_f32 v176, v159, v163, v162
	v_fma_f32 v164, |v176|, s17, v113
	v_fma_f32 v165, |v176|, s18, v114
	v_fma_f32 v166, |v176|, s19, v115
	v_lshrrev_b32_e32 v167, 26, v176
	v_min3_u32 v164, v164, v165, v166
	v_bfi_b32 v168, 31, v164, v167
	s_nop 1
	v_mul_u32_u24_dpp v170, v168, v180 quad_perm:[1,2,3,3] row_mask:0xf bank_mask:0xf bound_ctrl:1
	v_mad_u32_u24 v171, v168, v181, v170
	ds_write_b8_d16_hi v184, v171 offset:544
	s_barrier
	global_store_short_d16_hi v185, v176, s[48:49]
	s_waitcnt lgkmcnt(0)
	s_barrier
	ds_read_b128 v[122:125], v192 offset:544
	ds_read_b64 v[126:127], v192 offset:560
	ds_read_b128 v[128:131], v192 offset:672
	ds_read_b64 v[132:133], v192 offset:688
	s_nop 7
	s_waitcnt lgkmcnt(2)
	v_mfma_f32_16x16x128_f8f6f4 v[134:137], v[122:127], v[2:7], 0 cbsz:2 blgp:2
	v_mfma_f32_16x16x128_f8f6f4 v[138:141], v[122:127], v[14:19], 0 cbsz:2 blgp:2
	v_mfma_f32_16x16x128_f8f6f4 v[142:145], v[122:127], v[26:31], v[188:191] cbsz:2 blgp:2
	v_mfma_f32_16x16x128_f8f6f4 v[204:207], v[122:127], v[38:43], 0 cbsz:2 blgp:2
	v_mfma_f32_16x16x128_f8f6f4 v[208:211], v[122:127], v[50:55], 0 cbsz:2 blgp:2
	v_mfma_f32_16x16x128_f8f6f4 v[212:215], v[122:127], v[62:67], v[188:191] cbsz:2 blgp:2
	s_waitcnt lgkmcnt(0)
	v_mfma_f32_16x16x128_f8f6f4 v[134:137], v[128:133], v[8:13], v[134:137] cbsz:2 blgp:2
	v_mfma_f32_16x16x128_f8f6f4 v[204:207], v[128:133], v[44:49], v[204:207] cbsz:2 blgp:2
	v_mfma_f32_16x16x128_f8f6f4 v[138:141], v[128:133], v[20:25], v[138:141] cbsz:2 blgp:2
	v_mfma_f32_16x16x128_f8f6f4 v[208:211], v[128:133], v[56:61], v[208:211] cbsz:2 blgp:2
	v_mfma_f32_16x16x128_f8f6f4 v[142:145], v[128:133], v[32:37], v[142:145] cbsz:2 blgp:2
	v_mfma_f32_16x16x128_f8f6f4 v[212:215], v[128:133], v[68:73], v[212:215] cbsz:2 blgp:2
	v_cndmask_b32_e64 v158, v134, v204, s[0:1]
	v_cndmask_b32_e64 v159, v138, v208, s[0:1]
	v_fma_mix_f32 v158, v158, v100, v146 op_sel:[0,0,1] op_sel_hi:[0,0,1]
	v_fma_mix_f32 v159, v159, v101, v150 op_sel:[0,0,1] op_sel_hi:[0,0,1]
	v_exp_f32_e32 v158, v158
	v_exp_f32_e32 v159, v159
	v_fma_f32 v158, v158, v186, v186
	v_add_f32_e32 v159, 1.0, v159
	v_rcp_f32_e32 v158, v158
	v_rcp_f32_e32 v159, v159
	v_cndmask_b32_e64 v160, v142, v212, s[0:1]
	v_fma_mix_f32 v161, v158, v160, v154 op_sel:[0,0,1] op_sel_hi:[0,0,1]
	v_exp_f32_e32 v161, v161
	s_add_u32 s48, s48, s40
	v_add_f32_e32 v161, 1.0, v161
	v_rcp_f32_e32 v161, v161
	s_addc_u32 s49, s49, s41
	v_fma_f32 v162, v161, -2.0, 1.0
	v_sub_f32_e32 v163, v176, v162
	v_fma_f32 v176, v159, v163, v162
	v_fma_f32 v164, |v176|, s17, v113
	v_fma_f32 v165, |v176|, s18, v114
	v_fma_f32 v166, |v176|, s19, v115
	v_lshrrev_b32_e32 v167, 26, v176
	v_min3_u32 v164, v164, v165, v166
	v_bfi_b32 v168, 31, v164, v167
	s_nop 1
	v_mul_u32_u24_dpp v170, v168, v180 quad_perm:[1,2,3,3] row_mask:0xf bank_mask:0xf bound_ctrl:1
	v_mad_u32_u24 v171, v168, v181, v170
	ds_write_b8_d16_hi v184, v171
	s_barrier
	global_store_short_d16_hi v185, v176, s[48:49]
	s_waitcnt lgkmcnt(0)
	s_barrier
	ds_read_b128 v[122:125], v192 offset:0
	ds_read_b64 v[126:127], v192 offset:16
	ds_read_b128 v[128:131], v192 offset:128
	ds_read_b64 v[132:133], v192 offset:144
	s_nop 7
	s_waitcnt lgkmcnt(2)
	v_mfma_f32_16x16x128_f8f6f4 v[134:137], v[122:127], v[2:7], 0 cbsz:2 blgp:2
	v_mfma_f32_16x16x128_f8f6f4 v[138:141], v[122:127], v[14:19], 0 cbsz:2 blgp:2
	v_mfma_f32_16x16x128_f8f6f4 v[142:145], v[122:127], v[26:31], v[188:191] cbsz:2 blgp:2
	v_mfma_f32_16x16x128_f8f6f4 v[204:207], v[122:127], v[38:43], 0 cbsz:2 blgp:2
	v_mfma_f32_16x16x128_f8f6f4 v[208:211], v[122:127], v[50:55], 0 cbsz:2 blgp:2
	v_mfma_f32_16x16x128_f8f6f4 v[212:215], v[122:127], v[62:67], v[188:191] cbsz:2 blgp:2
	s_waitcnt lgkmcnt(0)
	v_mfma_f32_16x16x128_f8f6f4 v[134:137], v[128:133], v[8:13], v[134:137] cbsz:2 blgp:2
	v_mfma_f32_16x16x128_f8f6f4 v[204:207], v[128:133], v[44:49], v[204:207] cbsz:2 blgp:2
	v_mfma_f32_16x16x128_f8f6f4 v[138:141], v[128:133], v[20:25], v[138:141] cbsz:2 blgp:2
	v_mfma_f32_16x16x128_f8f6f4 v[208:211], v[128:133], v[56:61], v[208:211] cbsz:2 blgp:2
	v_mfma_f32_16x16x128_f8f6f4 v[142:145], v[128:133], v[32:37], v[142:145] cbsz:2 blgp:2
	v_mfma_f32_16x16x128_f8f6f4 v[212:215], v[128:133], v[68:73], v[212:215] cbsz:2 blgp:2
	v_cndmask_b32_e64 v158, v134, v204, s[0:1]
	v_cndmask_b32_e64 v159, v138, v208, s[0:1]
	v_fma_mix_f32 v158, v158, v100, v147 op_sel_hi:[0,0,1]
	v_fma_mix_f32 v159, v159, v101, v151 op_sel_hi:[0,0,1]
	v_exp_f32_e32 v158, v158
	v_exp_f32_e32 v159, v159
	v_fma_f32 v158, v158, v186, v186
	v_add_f32_e32 v159, 1.0, v159
	v_rcp_f32_e32 v158, v158
	v_rcp_f32_e32 v159, v159
	v_cndmask_b32_e64 v160, v142, v212, s[0:1]
	v_fma_mix_f32 v161, v158, v160, v155 op_sel_hi:[0,0,1]
	v_exp_f32_e32 v161, v161
	s_add_u32 s48, s48, s40
	v_add_f32_e32 v161, 1.0, v161
	v_rcp_f32_e32 v161, v161
	s_addc_u32 s49, s49, s41
	v_fma_f32 v162, v161, -2.0, 1.0
	v_sub_f32_e32 v163, v176, v162
	v_fma_f32 v176, v159, v163, v162
	v_fma_f32 v164, |v176|, s17, v113
	v_fma_f32 v165, |v176|, s18, v114
	v_fma_f32 v166, |v176|, s19, v115
	v_lshrrev_b32_e32 v167, 26, v176
	v_min3_u32 v164, v164, v165, v166
	v_bfi_b32 v168, 31, v164, v167
	s_nop 1
	v_mul_u32_u24_dpp v170, v168, v180 quad_perm:[1,2,3,3] row_mask:0xf bank_mask:0xf bound_ctrl:1
	v_mad_u32_u24 v171, v168, v181, v170
	ds_write_b8_d16_hi v184, v171 offset:544
	s_barrier
	global_store_short_d16_hi v185, v176, s[48:49]
	s_waitcnt lgkmcnt(0)
	s_barrier
	ds_read_b128 v[122:125], v192 offset:544
	ds_read_b64 v[126:127], v192 offset:560
	ds_read_b128 v[128:131], v192 offset:672
	ds_read_b64 v[132:133], v192 offset:688
	s_nop 7
	s_waitcnt lgkmcnt(2)
	v_mfma_f32_16x16x128_f8f6f4 v[134:137], v[122:127], v[2:7], 0 cbsz:2 blgp:2
	v_mfma_f32_16x16x128_f8f6f4 v[138:141], v[122:127], v[14:19], 0 cbsz:2 blgp:2
	v_mfma_f32_16x16x128_f8f6f4 v[142:145], v[122:127], v[26:31], v[188:191] cbsz:2 blgp:2
	v_mfma_f32_16x16x128_f8f6f4 v[204:207], v[122:127], v[38:43], 0 cbsz:2 blgp:2
	v_mfma_f32_16x16x128_f8f6f4 v[208:211], v[122:127], v[50:55], 0 cbsz:2 blgp:2
	v_mfma_f32_16x16x128_f8f6f4 v[212:215], v[122:127], v[62:67], v[188:191] cbsz:2 blgp:2
	s_waitcnt lgkmcnt(0)
	v_mfma_f32_16x16x128_f8f6f4 v[134:137], v[128:133], v[8:13], v[134:137] cbsz:2 blgp:2
	v_mfma_f32_16x16x128_f8f6f4 v[204:207], v[128:133], v[44:49], v[204:207] cbsz:2 blgp:2
	v_mfma_f32_16x16x128_f8f6f4 v[138:141], v[128:133], v[20:25], v[138:141] cbsz:2 blgp:2
	v_mfma_f32_16x16x128_f8f6f4 v[208:211], v[128:133], v[56:61], v[208:211] cbsz:2 blgp:2
	v_mfma_f32_16x16x128_f8f6f4 v[142:145], v[128:133], v[32:37], v[142:145] cbsz:2 blgp:2
	v_mfma_f32_16x16x128_f8f6f4 v[212:215], v[128:133], v[68:73], v[212:215] cbsz:2 blgp:2
	v_cndmask_b32_e64 v158, v134, v204, s[0:1]
	v_cndmask_b32_e64 v159, v138, v208, s[0:1]
	v_fma_mix_f32 v158, v158, v100, v147 op_sel:[0,0,1] op_sel_hi:[0,0,1]
	v_fma_mix_f32 v159, v159, v101, v151 op_sel:[0,0,1] op_sel_hi:[0,0,1]
	v_exp_f32_e32 v158, v158
	v_exp_f32_e32 v159, v159
	v_fma_f32 v158, v158, v186, v186
	v_add_f32_e32 v159, 1.0, v159
	v_rcp_f32_e32 v158, v158
	v_rcp_f32_e32 v159, v159
	v_cndmask_b32_e64 v160, v142, v212, s[0:1]
	v_fma_mix_f32 v161, v158, v160, v155 op_sel:[0,0,1] op_sel_hi:[0,0,1]
	v_exp_f32_e32 v161, v161
	s_add_u32 s48, s48, s40
	v_add_f32_e32 v161, 1.0, v161
	v_rcp_f32_e32 v161, v161
	s_addc_u32 s49, s49, s41
	v_fma_f32 v162, v161, -2.0, 1.0
	v_sub_f32_e32 v163, v176, v162
	v_fma_f32 v176, v159, v163, v162
	v_fma_f32 v164, |v176|, s17, v113
	v_fma_f32 v165, |v176|, s18, v114
	v_fma_f32 v166, |v176|, s19, v115
	v_lshrrev_b32_e32 v167, 26, v176
	v_min3_u32 v164, v164, v165, v166
	v_bfi_b32 v168, 31, v164, v167
	s_nop 1
	v_mul_u32_u24_dpp v170, v168, v180 quad_perm:[1,2,3,3] row_mask:0xf bank_mask:0xf bound_ctrl:1
	v_mad_u32_u24 v171, v168, v181, v170
	ds_write_b8_d16_hi v184, v171
	s_barrier
	global_store_short_d16_hi v185, v176, s[48:49]
	s_waitcnt lgkmcnt(0)
	s_barrier
	ds_read_b128 v[122:125], v192 offset:0
	ds_read_b64 v[126:127], v192 offset:16
	ds_read_b128 v[128:131], v192 offset:128
	ds_read_b64 v[132:133], v192 offset:144
	s_nop 7
	s_waitcnt lgkmcnt(2)
	v_mfma_f32_16x16x128_f8f6f4 v[134:137], v[122:127], v[2:7], 0 cbsz:2 blgp:2
	v_mfma_f32_16x16x128_f8f6f4 v[138:141], v[122:127], v[14:19], 0 cbsz:2 blgp:2
	v_mfma_f32_16x16x128_f8f6f4 v[142:145], v[122:127], v[26:31], v[188:191] cbsz:2 blgp:2
	v_mfma_f32_16x16x128_f8f6f4 v[204:207], v[122:127], v[38:43], 0 cbsz:2 blgp:2
	v_mfma_f32_16x16x128_f8f6f4 v[208:211], v[122:127], v[50:55], 0 cbsz:2 blgp:2
	v_mfma_f32_16x16x128_f8f6f4 v[212:215], v[122:127], v[62:67], v[188:191] cbsz:2 blgp:2
	s_waitcnt lgkmcnt(0)
	v_mfma_f32_16x16x128_f8f6f4 v[134:137], v[128:133], v[8:13], v[134:137] cbsz:2 blgp:2
	v_mfma_f32_16x16x128_f8f6f4 v[204:207], v[128:133], v[44:49], v[204:207] cbsz:2 blgp:2
	v_mfma_f32_16x16x128_f8f6f4 v[138:141], v[128:133], v[20:25], v[138:141] cbsz:2 blgp:2
	v_mfma_f32_16x16x128_f8f6f4 v[208:211], v[128:133], v[56:61], v[208:211] cbsz:2 blgp:2
	v_mfma_f32_16x16x128_f8f6f4 v[142:145], v[128:133], v[32:37], v[142:145] cbsz:2 blgp:2
	v_mfma_f32_16x16x128_f8f6f4 v[212:215], v[128:133], v[68:73], v[212:215] cbsz:2 blgp:2
	v_cndmask_b32_e64 v158, v134, v204, s[0:1]
	v_cndmask_b32_e64 v159, v138, v208, s[0:1]
	v_fma_mix_f32 v158, v158, v100, v148 op_sel_hi:[0,0,1]
	v_fma_mix_f32 v159, v159, v101, v152 op_sel_hi:[0,0,1]
	v_exp_f32_e32 v158, v158
	v_exp_f32_e32 v159, v159
	v_fma_f32 v158, v158, v186, v186
	v_add_f32_e32 v159, 1.0, v159
	v_rcp_f32_e32 v158, v158
	v_rcp_f32_e32 v159, v159
	v_cndmask_b32_e64 v160, v142, v212, s[0:1]
	v_fma_mix_f32 v161, v158, v160, v156 op_sel_hi:[0,0,1]
	v_exp_f32_e32 v161, v161
	s_add_u32 s48, s48, s40
	v_add_f32_e32 v161, 1.0, v161
	v_rcp_f32_e32 v161, v161
	s_addc_u32 s49, s49, s41
	v_fma_f32 v162, v161, -2.0, 1.0
	v_sub_f32_e32 v163, v176, v162
	v_fma_f32 v176, v159, v163, v162
	v_fma_f32 v164, |v176|, s17, v113
	v_fma_f32 v165, |v176|, s18, v114
	v_fma_f32 v166, |v176|, s19, v115
	v_lshrrev_b32_e32 v167, 26, v176
	v_min3_u32 v164, v164, v165, v166
	v_bfi_b32 v168, 31, v164, v167
	s_nop 1
	v_mul_u32_u24_dpp v170, v168, v180 quad_perm:[1,2,3,3] row_mask:0xf bank_mask:0xf bound_ctrl:1
	v_mad_u32_u24 v171, v168, v181, v170
	ds_write_b8_d16_hi v184, v171 offset:544
	s_barrier
	global_store_short_d16_hi v185, v176, s[48:49]
	s_waitcnt lgkmcnt(0)
	s_barrier
	ds_read_b128 v[122:125], v192 offset:544
	ds_read_b64 v[126:127], v192 offset:560
	ds_read_b128 v[128:131], v192 offset:672
	ds_read_b64 v[132:133], v192 offset:688
	s_nop 7
	s_waitcnt lgkmcnt(2)
	v_mfma_f32_16x16x128_f8f6f4 v[134:137], v[122:127], v[2:7], 0 cbsz:2 blgp:2
	v_mfma_f32_16x16x128_f8f6f4 v[138:141], v[122:127], v[14:19], 0 cbsz:2 blgp:2
	v_mfma_f32_16x16x128_f8f6f4 v[142:145], v[122:127], v[26:31], v[188:191] cbsz:2 blgp:2
	v_mfma_f32_16x16x128_f8f6f4 v[204:207], v[122:127], v[38:43], 0 cbsz:2 blgp:2
	v_mfma_f32_16x16x128_f8f6f4 v[208:211], v[122:127], v[50:55], 0 cbsz:2 blgp:2
	v_mfma_f32_16x16x128_f8f6f4 v[212:215], v[122:127], v[62:67], v[188:191] cbsz:2 blgp:2
	s_waitcnt lgkmcnt(0)
	v_mfma_f32_16x16x128_f8f6f4 v[134:137], v[128:133], v[8:13], v[134:137] cbsz:2 blgp:2
	v_mfma_f32_16x16x128_f8f6f4 v[204:207], v[128:133], v[44:49], v[204:207] cbsz:2 blgp:2
	v_mfma_f32_16x16x128_f8f6f4 v[138:141], v[128:133], v[20:25], v[138:141] cbsz:2 blgp:2
	v_mfma_f32_16x16x128_f8f6f4 v[208:211], v[128:133], v[56:61], v[208:211] cbsz:2 blgp:2
	v_mfma_f32_16x16x128_f8f6f4 v[142:145], v[128:133], v[32:37], v[142:145] cbsz:2 blgp:2
	v_mfma_f32_16x16x128_f8f6f4 v[212:215], v[128:133], v[68:73], v[212:215] cbsz:2 blgp:2
	v_cndmask_b32_e64 v158, v134, v204, s[0:1]
	v_cndmask_b32_e64 v159, v138, v208, s[0:1]
	v_fma_mix_f32 v158, v158, v100, v148 op_sel:[0,0,1] op_sel_hi:[0,0,1]
	v_fma_mix_f32 v159, v159, v101, v152 op_sel:[0,0,1] op_sel_hi:[0,0,1]
	v_exp_f32_e32 v158, v158
	v_exp_f32_e32 v159, v159
	v_fma_f32 v158, v158, v186, v186
	v_add_f32_e32 v159, 1.0, v159
	v_rcp_f32_e32 v158, v158
	v_rcp_f32_e32 v159, v159
	v_cndmask_b32_e64 v160, v142, v212, s[0:1]
	v_fma_mix_f32 v161, v158, v160, v156 op_sel:[0,0,1] op_sel_hi:[0,0,1]
	v_exp_f32_e32 v161, v161
	s_add_u32 s48, s48, s40
	v_add_f32_e32 v161, 1.0, v161
	v_rcp_f32_e32 v161, v161
	s_addc_u32 s49, s49, s41
	v_fma_f32 v162, v161, -2.0, 1.0
	v_sub_f32_e32 v163, v176, v162
	v_fma_f32 v176, v159, v163, v162
	v_fma_f32 v164, |v176|, s17, v113
	v_fma_f32 v165, |v176|, s18, v114
	v_fma_f32 v166, |v176|, s19, v115
	v_lshrrev_b32_e32 v167, 26, v176
	v_min3_u32 v164, v164, v165, v166
	v_bfi_b32 v168, 31, v164, v167
	s_nop 1
	v_mul_u32_u24_dpp v170, v168, v180 quad_perm:[1,2,3,3] row_mask:0xf bank_mask:0xf bound_ctrl:1
	v_mad_u32_u24 v171, v168, v181, v170
	ds_write_b8_d16_hi v184, v171
	s_barrier
	global_store_short_d16_hi v185, v176, s[48:49]
	s_waitcnt lgkmcnt(0)
	s_barrier
	ds_read_b128 v[122:125], v192 offset:0
	ds_read_b64 v[126:127], v192 offset:16
	ds_read_b128 v[128:131], v192 offset:128
	ds_read_b64 v[132:133], v192 offset:144
	s_nop 7
	s_waitcnt lgkmcnt(2)
	v_mfma_f32_16x16x128_f8f6f4 v[134:137], v[122:127], v[2:7], 0 cbsz:2 blgp:2
	v_mfma_f32_16x16x128_f8f6f4 v[138:141], v[122:127], v[14:19], 0 cbsz:2 blgp:2
	v_mfma_f32_16x16x128_f8f6f4 v[142:145], v[122:127], v[26:31], v[188:191] cbsz:2 blgp:2
	v_mfma_f32_16x16x128_f8f6f4 v[204:207], v[122:127], v[38:43], 0 cbsz:2 blgp:2
	v_mfma_f32_16x16x128_f8f6f4 v[208:211], v[122:127], v[50:55], 0 cbsz:2 blgp:2
	v_mfma_f32_16x16x128_f8f6f4 v[212:215], v[122:127], v[62:67], v[188:191] cbsz:2 blgp:2
	s_waitcnt lgkmcnt(0)
	v_mfma_f32_16x16x128_f8f6f4 v[134:137], v[128:133], v[8:13], v[134:137] cbsz:2 blgp:2
	v_mfma_f32_16x16x128_f8f6f4 v[204:207], v[128:133], v[44:49], v[204:207] cbsz:2 blgp:2
	v_mfma_f32_16x16x128_f8f6f4 v[138:141], v[128:133], v[20:25], v[138:141] cbsz:2 blgp:2
	v_mfma_f32_16x16x128_f8f6f4 v[208:211], v[128:133], v[56:61], v[208:211] cbsz:2 blgp:2
	v_mfma_f32_16x16x128_f8f6f4 v[142:145], v[128:133], v[32:37], v[142:145] cbsz:2 blgp:2
	v_mfma_f32_16x16x128_f8f6f4 v[212:215], v[128:133], v[68:73], v[212:215] cbsz:2 blgp:2
	v_cndmask_b32_e64 v158, v134, v204, s[0:1]
	v_cndmask_b32_e64 v159, v138, v208, s[0:1]
	v_fma_mix_f32 v158, v158, v100, v149 op_sel_hi:[0,0,1]
	v_fma_mix_f32 v159, v159, v101, v153 op_sel_hi:[0,0,1]
	v_exp_f32_e32 v158, v158
	v_exp_f32_e32 v159, v159
	v_fma_f32 v158, v158, v186, v186
	v_add_f32_e32 v159, 1.0, v159
	v_rcp_f32_e32 v158, v158
	v_rcp_f32_e32 v159, v159
	v_cndmask_b32_e64 v160, v142, v212, s[0:1]
	v_fma_mix_f32 v161, v158, v160, v157 op_sel_hi:[0,0,1]
	v_exp_f32_e32 v161, v161
	s_add_u32 s48, s48, s40
	v_add_f32_e32 v161, 1.0, v161
	v_rcp_f32_e32 v161, v161
	s_addc_u32 s49, s49, s41
	v_fma_f32 v162, v161, -2.0, 1.0
	v_sub_f32_e32 v163, v176, v162
	v_fma_f32 v176, v159, v163, v162
	v_fma_f32 v164, |v176|, s17, v113
	v_fma_f32 v165, |v176|, s18, v114
	v_fma_f32 v166, |v176|, s19, v115
	v_lshrrev_b32_e32 v167, 26, v176
	v_min3_u32 v164, v164, v165, v166
	v_bfi_b32 v168, 31, v164, v167
	s_nop 1
	v_mul_u32_u24_dpp v170, v168, v180 quad_perm:[1,2,3,3] row_mask:0xf bank_mask:0xf bound_ctrl:1
	v_mad_u32_u24 v171, v168, v181, v170
	ds_write_b8_d16_hi v184, v171 offset:544
	s_barrier
	global_store_short_d16_hi v185, v176, s[48:49]
	s_waitcnt lgkmcnt(0)
	s_barrier
	ds_read_b128 v[122:125], v192 offset:544
	ds_read_b64 v[126:127], v192 offset:560
	ds_read_b128 v[128:131], v192 offset:672
	ds_read_b64 v[132:133], v192 offset:688
	s_add_i32 s44, s44, 16
	s_nop 7
	s_waitcnt lgkmcnt(2)
	v_mfma_f32_16x16x128_f8f6f4 v[134:137], v[122:127], v[2:7], 0 cbsz:2 blgp:2
	v_mfma_f32_16x16x128_f8f6f4 v[138:141], v[122:127], v[14:19], 0 cbsz:2 blgp:2
	v_mfma_f32_16x16x128_f8f6f4 v[142:145], v[122:127], v[26:31], v[188:191] cbsz:2 blgp:2
	v_mfma_f32_16x16x128_f8f6f4 v[204:207], v[122:127], v[38:43], 0 cbsz:2 blgp:2
	v_mfma_f32_16x16x128_f8f6f4 v[208:211], v[122:127], v[50:55], 0 cbsz:2 blgp:2
	v_mfma_f32_16x16x128_f8f6f4 v[212:215], v[122:127], v[62:67], v[188:191] cbsz:2 blgp:2
	s_waitcnt lgkmcnt(0)
	v_mfma_f32_16x16x128_f8f6f4 v[134:137], v[128:133], v[8:13], v[134:137] cbsz:2 blgp:2
	v_mfma_f32_16x16x128_f8f6f4 v[204:207], v[128:133], v[44:49], v[204:207] cbsz:2 blgp:2
	v_mfma_f32_16x16x128_f8f6f4 v[138:141], v[128:133], v[20:25], v[138:141] cbsz:2 blgp:2
	v_mfma_f32_16x16x128_f8f6f4 v[208:211], v[128:133], v[56:61], v[208:211] cbsz:2 blgp:2
	v_mfma_f32_16x16x128_f8f6f4 v[142:145], v[128:133], v[32:37], v[142:145] cbsz:2 blgp:2
	v_mfma_f32_16x16x128_f8f6f4 v[212:215], v[128:133], v[68:73], v[212:215] cbsz:2 blgp:2
	v_cndmask_b32_e64 v158, v134, v204, s[0:1]
	v_cndmask_b32_e64 v159, v138, v208, s[0:1]
	v_fma_mix_f32 v158, v158, v100, v149 op_sel:[0,0,1] op_sel_hi:[0,0,1]
	v_fma_mix_f32 v159, v159, v101, v153 op_sel:[0,0,1] op_sel_hi:[0,0,1]
	v_exp_f32_e32 v158, v158
	v_exp_f32_e32 v159, v159
	v_fma_f32 v158, v158, v186, v186
	v_add_f32_e32 v159, 1.0, v159
	v_rcp_f32_e32 v158, v158
	v_rcp_f32_e32 v159, v159
	v_cndmask_b32_e64 v160, v142, v212, s[0:1]
	v_fma_mix_f32 v161, v158, v160, v157 op_sel:[0,0,1] op_sel_hi:[0,0,1]
	v_exp_f32_e32 v161, v161
	s_add_u32 s48, s48, s40
	v_add_f32_e32 v161, 1.0, v161
	v_rcp_f32_e32 v161, v161
	s_addc_u32 s49, s49, s41
	v_fma_f32 v162, v161, -2.0, 1.0
	v_sub_f32_e32 v163, v176, v162
	v_fma_f32 v176, v159, v163, v162
	v_fma_f32 v164, |v176|, s17, v113
	v_fma_f32 v165, |v176|, s18, v114
	v_fma_f32 v166, |v176|, s19, v115
	v_lshrrev_b32_e32 v167, 26, v176
	v_min3_u32 v164, v164, v165, v166
	v_bfi_b32 v168, 31, v164, v167
	s_nop 1
	v_mul_u32_u24_dpp v170, v168, v180 quad_perm:[1,2,3,3] row_mask:0xf bank_mask:0xf bound_ctrl:1
	v_mad_u32_u24 v171, v168, v181, v170
	ds_write_b8_d16_hi v184, v171
	s_barrier
	global_store_short_d16_hi v185, v176, s[48:49]
	s_cmp_lt_i32 s44, s45
	s_cbranch_scc1 .Lscan_loop_b_f2
	s_waitcnt lgkmcnt(0)
	s_barrier
